# speedup vs baseline: 1.0451x; 1.0451x over previous
.LBB0_106:
	s_mov_b64 exec, -1
	s_waitcnt vmcnt(0) lgkmcnt(0)
	s_barrier
	s_cmp_ge_u32 s20, 0x61a80
	s_cbranch_scc1 .Lpl_end
	v_subrev_u32_e32 v0, s6, v2
	v_lshlrev_b32_e32 v1, 3, v0
	ds_read_b64 v[4:5], v1 offset:14336
	ds_read_b32 v6, v1 offset:14344
	v_mov_b32_e32 v7, s21
	v_cmp_eq_u32_e32 vcc, 0xff, v0
	s_waitcnt lgkmcnt(0)
	s_nop 1
	v_cndmask_b32_e32 v6, v6, v7, vcc
	v_sub_u32_e32 v8, v5, v4
	v_sub_u32_e32 v9, v6, v5
	v_max_u32_e32 v10, v8, v9
	s_nop 1
	v_max_u32_dpp v10, v10, v10 quad_perm:[1,0,3,2] row_mask:0xf bank_mask:0xf
	s_nop 1
	v_max_u32_dpp v10, v10, v10 quad_perm:[2,3,0,1] row_mask:0xf bank_mask:0xf
	s_nop 1
	v_max_u32_dpp v10, v10, v10 row_half_mirror row_mask:0xf bank_mask:0xf
	v_lshrrev_b32_e32 v11, 3, v0
	s_lshr_b32 s0, s20, 4
	v_add_u32_e32 v11, s0, v11
	s_movk_i32 s1, 0x61a8
	v_cmp_gt_u32_e64 s[2:3], s1, v11
	s_add_u32 s14, s10, 0x712bd00
	s_addc_u32 s15, s11, 0
	s_add_u32 s16, s14, 0x186a000
	s_addc_u32 s17, s15, 0
	v_and_b32_e32 v12, 7, v0
	v_cmp_eq_u32_e32 vcc, 0, v12
	s_and_b64 s[4:5], vcc, s[2:3]
	v_lshlrev_b32_e32 v22, 2, v11
	s_and_saveexec_b64 s[12:13], s[4:5]
	s_cbranch_execz .Lpl_nom
	global_store_dword v22, v10, s[16:17]
.Lpl_nom:
	s_mov_b64 exec, s[12:13]
	v_min_u32_e32 v13, 16, v10
	v_lshlrev_b32_e32 v14, 10, v11
	v_lshlrev_b32_e32 v15, 1, v0
	v_and_b32_e32 v15, 15, v15
	v_lshl_add_u32 v14, v15, 2, v14
	v_mov_b32_e32 v20, 0
	v_mov_b32_e32 v21, 0x800000
	v_lshlrev_b32_e32 v16, 2, v4
	v_lshlrev_b32_e32 v17, 2, v5
	s_cmpk_lt_i32 s21, 0xc01
	s_cbranch_scc1 .Lpl_small
	v_add_u32_e32 v16, s6, v4
	v_add_u32_e32 v17, s6, v5
	v_lshlrev_b32_e32 v16, 2, v16
	v_lshlrev_b32_e32 v17, 2, v17
.Lpl_small:
	s_and_b64 exec, exec, s[2:3]
	s_cbranch_execz .Lpl_end
.Lpl_loop:
	v_cmp_lt_u32_e32 vcc, v20, v13
	s_and_b64 exec, exec, vcc
	s_cbranch_execz .Lpl_end
	s_cmpk_lt_i32 s21, 0xc01
	s_cbranch_scc0 .Lpl_big
	ds_read_b32 v18, v16
	ds_read_b32 v19, v17
	s_waitcnt lgkmcnt(0)
	s_branch .Lpl_sel
.Lpl_big:
	global_load_dword v18, v16, s[10:11] sc1
	global_load_dword v19, v17, s[10:11] sc1
	s_waitcnt vmcnt(0)
.Lpl_sel:
	v_cmp_lt_u32_e32 vcc, v20, v8
	v_add_u32_e32 v16, 4, v16
	v_add_u32_e32 v17, 4, v17
	v_cndmask_b32_e32 v18, v21, v18, vcc
	v_cmp_lt_u32_e32 vcc, v20, v9
	v_add_u32_e32 v20, 1, v20
	s_nop 0
	v_cndmask_b32_e32 v19, v21, v19, vcc
	global_store_dwordx2 v14, v[18:19], s[14:15]
	v_add_u32_e32 v14, 64, v14
	s_branch .Lpl_loop

_Z12k_layer_pool9LayerArgs:
	s_load_dwordx8 s[4:11], s[0:1], 0x0
	s_load_dwordx8 s[12:19], s[0:1], 0x20
	s_load_dwordx2 s[22:23], s[0:1], 0x60
	s_load_dwordx2 s[30:31], s[0:1], 0x58
	v_and_b32_e32 v159, 63, v0
	v_lshrrev_b32_e32 v160, 6, v0
	v_and_b32_e32 v143, 3, v159
	v_and_b32_e32 v167, 15, v159
	s_nop 0
	v_readfirstlane_b32 s61, v160
	s_waitcnt lgkmcnt(0)
	s_mov_b64 s[26:27], s[6:7]
	s_mov_b64 s[28:29], s[10:11]
	s_mov_b64 s[24:25], s[14:15]
	s_mov_b64 s[64:65], s[16:17]
	s_mov_b64 s[66:67], s[18:19]
	s_mov_b64 s[68:69], s[8:9]
	s_mov_b32 s8, s4
	s_and_b32 s9, s5, 0xffff
	s_mov_b32 s10, 0x40000000
	s_mov_b32 s11, 0x20000
	s_mov_b32 s12, s68
	s_and_b32 s13, s69, 0xffff
	s_mov_b32 s14, 0x40000000
	s_mov_b32 s15, 0x20000
	s_add_u32 s16, s24, 0x712bd00
	s_addc_u32 s17, s25, 0
	s_add_u32 s18, s16, 0xc35000
	s_addc_u32 s19, s17, 0
	s_add_u32 s20, s16, 0x186a000
	s_addc_u32 s21, s17, 0
	s_mul_i32 s52, s2, 49
	s_add_u32 s32, s52, 49
	s_min_u32 s32, s32, 12500
	s_mov_b32 s40, s64
	s_and_b32 s41, s65, 0xffff
	s_mov_b32 s42, 0x18000
	s_mov_b32 s43, 0x20000
	v_lshlrev_b32_e32 v160, 4, v0
	buffer_load_dwordx4 v[2:5], v160, s[40:43], 0 offen
	v_add_u32_e32 v161, 0x3000, v160
	buffer_load_dwordx4 v[6:9], v161, s[40:43], 0 offen
	v_add_u32_e32 v161, 0x6000, v160
	buffer_load_dwordx4 v[10:13], v161, s[40:43], 0 offen
	v_add_u32_e32 v161, 0x9000, v160
	buffer_load_dwordx4 v[14:17], v161, s[40:43], 0 offen
	v_add_u32_e32 v161, 0xc000, v160
	buffer_load_dwordx4 v[18:21], v161, s[40:43], 0 offen
	v_add_u32_e32 v161, 0xf000, v160
	buffer_load_dwordx4 v[22:25], v161, s[40:43], 0 offen
	v_add_u32_e32 v161, 0x12000, v160
	buffer_load_dwordx4 v[26:29], v161, s[40:43], 0 offen
	v_add_u32_e32 v161, 0x15000, v160
	buffer_load_dwordx4 v[30:33], v161, s[40:43], 0 offen
	v_lshlrev_b32_e32 v162, 2, v0
	v_cmp_gt_u32_e32 vcc, 0x80, v0
	s_and_saveexec_b64 s[58:59], vcc
	s_cbranch_execz .Lfp_nobias
	global_load_dword v163, v162, s[66:67]
.Lfp_nobias:
	s_mov_b64 exec, s[58:59]
	v_mov_b32_e32 v151, 0
	v_add_u32_e32 v152, 0x24e00, v162
	ds_write_b32 v152, v151
	v_cmp_gt_u32_e32 vcc, 0x100, v0
	s_and_saveexec_b64 s[58:59], vcc
	ds_write_b32 v152, v151 offset:3072
	s_mov_b64 exec, s[58:59]
	s_lshl_b32 s53, s52, 6
	s_load_dword s60, s[30:31], s53
	s_waitcnt vmcnt(7)
	ds_write_b128 v160, v[2:5]
	s_waitcnt vmcnt(6)
	v_add_u32_e32 v161, 0x3000, v160
	ds_write_b128 v161, v[6:9]
	s_waitcnt vmcnt(5)
	v_add_u32_e32 v161, 0x6000, v160
	ds_write_b128 v161, v[10:13]
	s_waitcnt vmcnt(4)
	v_add_u32_e32 v161, 0x9000, v160
	ds_write_b128 v161, v[14:17]
	s_waitcnt vmcnt(3)
	v_add_u32_e32 v161, 0xc000, v160
	ds_write_b128 v161, v[18:21]
	s_waitcnt vmcnt(2)
	v_add_u32_e32 v161, 0xf000, v160
	ds_write_b128 v161, v[22:25]
	s_waitcnt vmcnt(1)
	v_add_u32_e32 v161, 0x12000, v160
	ds_write_b128 v161, v[26:29]
	s_waitcnt vmcnt(0)
	v_add_u32_e32 v161, 0x15000, v160
	ds_write_b128 v161, v[30:33]
	s_waitcnt vmcnt(0)
	v_cmp_gt_u32_e32 vcc, 0x80, v0
	s_and_saveexec_b64 s[58:59], vcc
	v_add_u32_e32 v162, 0x24c00, v162
	ds_write_b32 v162, v163
	s_mov_b64 exec, s[58:59]
	v_cmp_eq_u32_e32 vcc, 0, v0
	s_and_saveexec_b64 s[58:59], vcc
	v_mov_b32_e32 v160, 0x25e00
	v_mov_b32_e32 v161, s52
	ds_write_b32 v160, v161
	s_mov_b64 exec, s[58:59]
	s_waitcnt lgkmcnt(0)
	s_barrier
	s_mul_i32 s61, s61, 0x1100
	s_add_u32 s61, s61, 0x18000
	v_lshrrev_b32_e32 v160, 2, v159
	v_lshrrev_b32_e32 v161, 4, v159
	v_lshlrev_b32_e32 v134, 4, v143
	v_mov_b32_e32 v135, v134
	v_mul_u32_u24_e32 v162, 0x110, v160
	v_add3_u32 v136, v162, v134, s61
	v_mul_u32_u24_e32 v162, 0x110, v167
	v_lshl_add_u32 v137, v161, 4, v162
	v_add_u32_e32 v137, s61, v137
	v_lshl_add_u32 v140, v161, 3, v162
	v_add_u32_e32 v140, s61, v140
	v_mul_u32_u24_e32 v162, 0x110, v161
	v_lshl_add_u32 v141, v167, 4, v162
	v_add_u32_e32 v141, s61, v141
	v_lshlrev_b32_e32 v138, 4, v159
	v_add_u32_e32 v139, 0x10000, v138
	v_lshlrev_b32_e32 v142, 8, v161
	v_lshl_add_u32 v142, v167, 4, v142
	v_mov_b32_e32 v144, 0x800000
	v_lshlrev_b32_e32 v145, 2, v160
	v_lshl_add_u32 v145, v143, 6, v145
	v_mul_u32_u24_e32 v146, 0x100, v160
	v_add_u32_e32 v146, v146, v135
	v_mov_b32_e32 v160, 1
	v_mov_b32_e32 v161, 0x25e00
	s_mov_b64 s[58:59], exec
	s_mov_b64 exec, 1
	ds_add_rtn_u32 v160, v161, v160
	s_waitcnt lgkmcnt(0)
	v_readfirstlane_b32 s35, v160
	s_mov_b64 exec, s[58:59]
	s_lshl_b32 s52, s35, 10
	v_add_u32_e32 v160, s52, v145
	global_load_dword v151, v160, s[16:17]
	global_load_dword v152, v160, s[16:17] offset:256
	global_load_dword v153, v160, s[18:19]
	global_load_dword v154, v160, s[18:19] offset:256
	s_lshl_b32 s52, s35, 2
	v_and_b32_e32 v161, 1, v159
	v_mul_u32_u24_e32 v161, 0xc350, v161
	v_add_u32_e32 v161, s52, v161
	global_load_dword v155, v161, s[20:21]
	s_min_u32 s52, s35, 12499
	s_lshl_b32 s52, s52, 6
	v_lshl_add_u32 v161, v167, 2, s52
	global_load_dword v164, v161, s[30:31]
	s_waitcnt vmcnt(0)
	s_mov_b32 s34, s35
	v_readlane_b32 s52, v155, 0
	v_readlane_b32 s53, v155, 1
	s_cmp_lt_u32 s34, s32
	s_cselect_b32 s47, s52, 0
	s_cselect_b32 s48, s53, 0
	s_max_u32 s38, s47, 2
	s_max_u32 s39, s48, 2
	v_cmp_gt_i32_e32 vcc, s47, v143
	s_nop 1
	v_cndmask_b32_e32 v147, v144, v151, vcc
	v_mov_b32_e32 v148, v152
	v_mov_b32_e32 v149, v153
	v_mov_b32_e32 v150, v154
	v_mov_b32_e32 v165, v164
	s_mov_b32 s44, 0
	s_mov_b32 s46, 0
	s_mov_b32 s45, s38
	s_mov_b64 s[40:41], s[8:9]
	s_mov_b64 s[42:43], s[10:11]
	s_movk_i32 s49, 0x100
	s_mov_b32 s70, 0
	v_mov_b32_e32 v160, 1
	v_mov_b32_e32 v161, 0x25e00
	s_mov_b64 s[58:59], exec
	s_mov_b64 exec, 1
	ds_add_rtn_u32 v160, v161, v160
	s_waitcnt lgkmcnt(0)
	v_readfirstlane_b32 s35, v160
	s_mov_b64 exec, s[58:59]
	s_lshl_b32 s52, s35, 10
	v_add_u32_e32 v160, s52, v145
	global_load_dword v151, v160, s[16:17]
	global_load_dword v152, v160, s[16:17] offset:256
	global_load_dword v153, v160, s[18:19]
	global_load_dword v154, v160, s[18:19] offset:256
	s_lshl_b32 s52, s35, 2
	v_and_b32_e32 v161, 1, v159
	v_mul_u32_u24_e32 v161, 0xc350, v161
	v_add_u32_e32 v161, s52, v161
	global_load_dword v155, v161, s[20:21]
	s_min_u32 s52, s35, 12499
	s_lshl_b32 s52, s52, 6
	v_lshl_add_u32 v161, v167, 2, s52
	global_load_dword v164, v161, s[30:31]
	s_waitcnt lgkmcnt(0)
	s_mov_b32 s64, 2
	s_mov_b32 s66, 0
.Lfp_tilestart:
	s_mov_b32 s33, s34
	s_mov_b32 s65, s38
	s_mov_b32 s37, s39
	v_mov_b32_e32 v166, v165
	s_cmp_ge_u32 s33, s32
	s_cbranch_scc1 .Lfp_exit
	v_mov_b32_e32 v66, 0
	v_mov_b32_e32 v67, 0
	v_mov_b32_e32 v68, 0
	v_mov_b32_e32 v69, 0
	v_mov_b32_e32 v70, 0
	v_mov_b32_e32 v71, 0
	v_mov_b32_e32 v72, 0
	v_mov_b32_e32 v73, 0
	v_mov_b32_e32 v74, 0
	v_mov_b32_e32 v75, 0
	v_mov_b32_e32 v76, 0
	v_mov_b32_e32 v77, 0
	v_mov_b32_e32 v78, 0
	v_mov_b32_e32 v79, 0
	v_mov_b32_e32 v80, 0
	v_mov_b32_e32 v81, 0
	v_lshlrev_b32_e32 v163, 2, v167
	v_add_u32_e32 v163, 0x24c00, v163
	ds_read_b32 v82, v163 offset:0
	ds_read_b32 v86, v163 offset:64
	ds_read_b32 v90, v163 offset:128
	ds_read_b32 v94, v163 offset:192
	ds_read_b32 v98, v163 offset:256
	ds_read_b32 v102, v163 offset:320
	ds_read_b32 v106, v163 offset:384
	ds_read_b32 v110, v163 offset:448
	s_waitcnt lgkmcnt(0)
	v_mov_b32_e32 v83, v82
	v_mov_b32_e32 v84, v82
	v_mov_b32_e32 v85, v82
	v_mov_b32_e32 v87, v86
	v_mov_b32_e32 v88, v86
	v_mov_b32_e32 v89, v86
	v_mov_b32_e32 v91, v90
	v_mov_b32_e32 v92, v90
	v_mov_b32_e32 v93, v90
	v_mov_b32_e32 v95, v94
	v_mov_b32_e32 v96, v94
	v_mov_b32_e32 v97, v94
	v_mov_b32_e32 v99, v98
	v_mov_b32_e32 v100, v98
	v_mov_b32_e32 v101, v98
	v_mov_b32_e32 v103, v102
	v_mov_b32_e32 v104, v102
	v_mov_b32_e32 v105, v102
	v_mov_b32_e32 v107, v106
	v_mov_b32_e32 v108, v106
	v_mov_b32_e32 v109, v106
	v_mov_b32_e32 v111, v110
	v_mov_b32_e32 v112, v110
	v_mov_b32_e32 v113, v110
	s_cmp_eq_u32 s64, 2
	s_cbranch_scc1 .Lfp_st_0
	s_mov_b32 s64, 0
	s_cmp_eq_u32 s51, 0
	s_cbranch_scc1 .Lfp_is_0
	s_cmp_eq_u32 s51, 1
	s_cbranch_scc1 .Lfp_is_1
	s_cmp_eq_u32 s51, 2
	s_cbranch_scc1 .Lfp_is_2
	s_branch .Lfp_is_3
.Lfp_st_0:
	s_cmp_eq_u32 s64, 0
	s_cbranch_scc1 .Lfp_ad_0
	s_cmp_eq_u32 s64, 1
	s_cbranch_scc0 .Lfp_is_0
	s_waitcnt vmcnt(12)
	ds_write_b128 v136, v[2:5]
	ds_write_b128 v136, v[6:9] offset:64
	ds_write_b128 v136, v[10:13] offset:128
	ds_write_b128 v136, v[14:17] offset:192
	s_mov_b32 s51, 0
	s_branch .Lfp_tileend
.Lfp_ad_0:
	s_waitcnt vmcnt(12)
	v_pk_add_f16 v66, v66, v2
	v_pk_add_f16 v67, v67, v3
	v_pk_add_f16 v68, v68, v4
	v_pk_add_f16 v69, v69, v5
	v_pk_add_f16 v70, v70, v6
	v_pk_add_f16 v71, v71, v7
	v_pk_add_f16 v72, v72, v8
	v_pk_add_f16 v73, v73, v9
	v_pk_add_f16 v74, v74, v10
	v_pk_add_f16 v75, v75, v11
	v_pk_add_f16 v76, v76, v12
	v_pk_add_f16 v77, v77, v13
	v_pk_add_f16 v78, v78, v14
	v_pk_add_f16 v79, v79, v15
	v_pk_add_f16 v80, v80, v16
	v_pk_add_f16 v81, v81, v17
	s_sub_u32 s65, s65, 1
	s_cmp_eq_u32 s65, 0
	s_cbranch_scc0 .Lfp_is_0
	s_mov_b32 s51, 0
	s_branch .Lfp_partend
.Lfp_is_0:
	s_cmp_eq_u32 s44, 2
	s_cbranch_scc1 .Lfp_iself_0
	s_nop 1
	v_mov_b32_dpp v157, v147 quad_perm:[0,0,0,0] row_mask:0xf bank_mask:0xf
	v_mov_b32_dpp v147, v147 quad_perm:[1,2,3,0] row_mask:0xf bank_mask:0xf
	v_mad_u32_u24 v158, v157, s49, v134
	v_or_b32_e32 v160, s70, v158
	buffer_load_dwordx4 v[2:5], v158, s[40:43], 0 offen
	buffer_load_dwordx4 v[6:9], v158, s[40:43], 0 offen offset:64
	buffer_load_dwordx4 v[10:13], v158, s[40:43], 0 offen offset:128
	buffer_load_dwordx4 v[14:17], v160, s[40:43], 0 offen offset:192
	s_add_u32 s46, s46, 1
	s_sub_u32 s45, s45, 1
	s_mov_b32 s51, 0
	s_cmp_eq_u32 s45, 0
	s_cbranch_scc1 .Lfp_ipe
	s_and_b32 s52, s46, 3
	s_cmp_eq_u32 s52, 0
	s_cbranch_scc1 .Lfp_iq
	s_branch .Lfp_nx_0
.Lfp_iself_0:
	s_mul_i32 s52, s34, 0x1000
	v_add_u32_e32 v158, s52, v146
	buffer_load_dwordx4 v[2:5], v158, s[12:15], 0 offen
	buffer_load_dwordx4 v[6:9], v158, s[12:15], 0 offen offset:64
	buffer_load_dwordx4 v[10:13], v158, s[12:15], 0 offen offset:128
	buffer_load_dwordx4 v[14:17], v158, s[12:15], 0 offen offset:192
	s_mov_b32 s51, 0
	s_branch .Lfp_ien
.Lfp_nx_0:
.Lfp_st_1:
	s_cmp_eq_u32 s64, 0
	s_cbranch_scc1 .Lfp_ad_1
	s_cmp_eq_u32 s64, 1
	s_cbranch_scc0 .Lfp_is_1
	s_waitcnt vmcnt(12)
	ds_write_b128 v136, v[18:21]
	ds_write_b128 v136, v[22:25] offset:64
	ds_write_b128 v136, v[26:29] offset:128
	ds_write_b128 v136, v[30:33] offset:192
	s_mov_b32 s51, 1
	s_branch .Lfp_tileend
.Lfp_ad_1:
	s_waitcnt vmcnt(12)
	v_pk_add_f16 v66, v66, v18
	v_pk_add_f16 v67, v67, v19
	v_pk_add_f16 v68, v68, v20
	v_pk_add_f16 v69, v69, v21
	v_pk_add_f16 v70, v70, v22
	v_pk_add_f16 v71, v71, v23
	v_pk_add_f16 v72, v72, v24
	v_pk_add_f16 v73, v73, v25
	v_pk_add_f16 v74, v74, v26
	v_pk_add_f16 v75, v75, v27
	v_pk_add_f16 v76, v76, v28
	v_pk_add_f16 v77, v77, v29
	v_pk_add_f16 v78, v78, v30
	v_pk_add_f16 v79, v79, v31
	v_pk_add_f16 v80, v80, v32
	v_pk_add_f16 v81, v81, v33
	s_sub_u32 s65, s65, 1
	s_cmp_eq_u32 s65, 0
	s_cbranch_scc0 .Lfp_is_1
	s_mov_b32 s51, 1
	s_branch .Lfp_partend
.Lfp_is_1:
	s_cmp_eq_u32 s44, 2
	s_cbranch_scc1 .Lfp_iself_1
	s_nop 1
	v_mov_b32_dpp v157, v147 quad_perm:[0,0,0,0] row_mask:0xf bank_mask:0xf
	v_mov_b32_dpp v147, v147 quad_perm:[1,2,3,0] row_mask:0xf bank_mask:0xf
	v_mad_u32_u24 v158, v157, s49, v134
	v_or_b32_e32 v160, s70, v158
	buffer_load_dwordx4 v[18:21], v158, s[40:43], 0 offen
	buffer_load_dwordx4 v[22:25], v158, s[40:43], 0 offen offset:64
	buffer_load_dwordx4 v[26:29], v158, s[40:43], 0 offen offset:128
	buffer_load_dwordx4 v[30:33], v160, s[40:43], 0 offen offset:192
	s_add_u32 s46, s46, 1
	s_sub_u32 s45, s45, 1
	s_mov_b32 s51, 1
	s_cmp_eq_u32 s45, 0
	s_cbranch_scc1 .Lfp_ipe
	s_and_b32 s52, s46, 3
	s_cmp_eq_u32 s52, 0
	s_cbranch_scc1 .Lfp_iq
	s_branch .Lfp_nx_1
.Lfp_iself_1:
	s_mul_i32 s52, s34, 0x1000
	v_add_u32_e32 v158, s52, v146
	buffer_load_dwordx4 v[18:21], v158, s[12:15], 0 offen
	buffer_load_dwordx4 v[22:25], v158, s[12:15], 0 offen offset:64
	buffer_load_dwordx4 v[26:29], v158, s[12:15], 0 offen offset:128
	buffer_load_dwordx4 v[30:33], v158, s[12:15], 0 offen offset:192
	s_mov_b32 s51, 1
	s_branch .Lfp_ien
.Lfp_nx_1:
.Lfp_st_2:
	s_cmp_eq_u32 s64, 0
	s_cbranch_scc1 .Lfp_ad_2
	s_cmp_eq_u32 s64, 1
	s_cbranch_scc0 .Lfp_is_2
	s_waitcnt vmcnt(12)
	ds_write_b128 v136, v[34:37]
	ds_write_b128 v136, v[38:41] offset:64
	ds_write_b128 v136, v[42:45] offset:128
	ds_write_b128 v136, v[46:49] offset:192
	s_mov_b32 s51, 2
	s_branch .Lfp_tileend
.Lfp_ad_2:
	s_waitcnt vmcnt(12)
	v_pk_add_f16 v66, v66, v34
	v_pk_add_f16 v67, v67, v35
	v_pk_add_f16 v68, v68, v36
	v_pk_add_f16 v69, v69, v37
	v_pk_add_f16 v70, v70, v38
	v_pk_add_f16 v71, v71, v39
	v_pk_add_f16 v72, v72, v40
	v_pk_add_f16 v73, v73, v41
	v_pk_add_f16 v74, v74, v42
	v_pk_add_f16 v75, v75, v43
	v_pk_add_f16 v76, v76, v44
	v_pk_add_f16 v77, v77, v45
	v_pk_add_f16 v78, v78, v46
	v_pk_add_f16 v79, v79, v47
	v_pk_add_f16 v80, v80, v48
	v_pk_add_f16 v81, v81, v49
	s_sub_u32 s65, s65, 1
	s_cmp_eq_u32 s65, 0
	s_cbranch_scc0 .Lfp_is_2
	s_mov_b32 s51, 2
	s_branch .Lfp_partend
.Lfp_is_2:
	s_cmp_eq_u32 s44, 2
	s_cbranch_scc1 .Lfp_iself_2
	s_nop 1
	v_mov_b32_dpp v157, v147 quad_perm:[0,0,0,0] row_mask:0xf bank_mask:0xf
	v_mov_b32_dpp v147, v147 quad_perm:[1,2,3,0] row_mask:0xf bank_mask:0xf
	v_mad_u32_u24 v158, v157, s49, v134
	v_or_b32_e32 v160, s70, v158
	buffer_load_dwordx4 v[34:37], v158, s[40:43], 0 offen
	buffer_load_dwordx4 v[38:41], v158, s[40:43], 0 offen offset:64
	buffer_load_dwordx4 v[42:45], v158, s[40:43], 0 offen offset:128
	buffer_load_dwordx4 v[46:49], v160, s[40:43], 0 offen offset:192
	s_add_u32 s46, s46, 1
	s_sub_u32 s45, s45, 1
	s_mov_b32 s51, 2
	s_cmp_eq_u32 s45, 0
	s_cbranch_scc1 .Lfp_ipe
	s_and_b32 s52, s46, 3
	s_cmp_eq_u32 s52, 0
	s_cbranch_scc1 .Lfp_iq
	s_branch .Lfp_nx_2
.Lfp_iself_2:
	s_mul_i32 s52, s34, 0x1000
	v_add_u32_e32 v158, s52, v146
	buffer_load_dwordx4 v[34:37], v158, s[12:15], 0 offen
	buffer_load_dwordx4 v[38:41], v158, s[12:15], 0 offen offset:64
	buffer_load_dwordx4 v[42:45], v158, s[12:15], 0 offen offset:128
	buffer_load_dwordx4 v[46:49], v158, s[12:15], 0 offen offset:192
	s_mov_b32 s51, 2
	s_branch .Lfp_ien
.Lfp_nx_2:
.Lfp_st_3:
	s_cmp_eq_u32 s64, 0
	s_cbranch_scc1 .Lfp_ad_3
	s_cmp_eq_u32 s64, 1
	s_cbranch_scc0 .Lfp_is_3
	s_waitcnt vmcnt(12)
	ds_write_b128 v136, v[50:53]
	ds_write_b128 v136, v[54:57] offset:64
	ds_write_b128 v136, v[58:61] offset:128
	ds_write_b128 v136, v[62:65] offset:192
	s_mov_b32 s51, 3
	s_branch .Lfp_tileend
.Lfp_ad_3:
	s_waitcnt vmcnt(12)
	v_pk_add_f16 v66, v66, v50
	v_pk_add_f16 v67, v67, v51
	v_pk_add_f16 v68, v68, v52
	v_pk_add_f16 v69, v69, v53
	v_pk_add_f16 v70, v70, v54
	v_pk_add_f16 v71, v71, v55
	v_pk_add_f16 v72, v72, v56
	v_pk_add_f16 v73, v73, v57
	v_pk_add_f16 v74, v74, v58
	v_pk_add_f16 v75, v75, v59
	v_pk_add_f16 v76, v76, v60
	v_pk_add_f16 v77, v77, v61
	v_pk_add_f16 v78, v78, v62
	v_pk_add_f16 v79, v79, v63
	v_pk_add_f16 v80, v80, v64
	v_pk_add_f16 v81, v81, v65
	s_sub_u32 s65, s65, 1
	s_cmp_eq_u32 s65, 0
	s_cbranch_scc0 .Lfp_is_3
	s_mov_b32 s51, 3
	s_branch .Lfp_partend
.Lfp_is_3:
	s_cmp_eq_u32 s44, 2
	s_cbranch_scc1 .Lfp_iself_3
	s_nop 1
	v_mov_b32_dpp v157, v147 quad_perm:[0,0,0,0] row_mask:0xf bank_mask:0xf
	v_mov_b32_dpp v147, v147 quad_perm:[1,2,3,0] row_mask:0xf bank_mask:0xf
	v_mad_u32_u24 v158, v157, s49, v134
	v_or_b32_e32 v160, s70, v158
	buffer_load_dwordx4 v[50:53], v158, s[40:43], 0 offen
	buffer_load_dwordx4 v[54:57], v158, s[40:43], 0 offen offset:64
	buffer_load_dwordx4 v[58:61], v158, s[40:43], 0 offen offset:128
	buffer_load_dwordx4 v[62:65], v160, s[40:43], 0 offen offset:192
	s_add_u32 s46, s46, 1
	s_sub_u32 s45, s45, 1
	s_mov_b32 s51, 3
	s_cmp_eq_u32 s45, 0
	s_cbranch_scc1 .Lfp_ipe
	s_and_b32 s52, s46, 3
	s_cmp_eq_u32 s52, 0
	s_cbranch_scc1 .Lfp_iq
	s_branch .Lfp_nx_3
.Lfp_iself_3:
	s_mul_i32 s52, s34, 0x1000
	v_add_u32_e32 v158, s52, v146
	buffer_load_dwordx4 v[50:53], v158, s[12:15], 0 offen
	buffer_load_dwordx4 v[54:57], v158, s[12:15], 0 offen offset:64
	buffer_load_dwordx4 v[58:61], v158, s[12:15], 0 offen offset:128
	buffer_load_dwordx4 v[62:65], v158, s[12:15], 0 offen offset:192
	s_mov_b32 s51, 3
	s_branch .Lfp_ien
.Lfp_nx_3:
	s_cmp_eq_u32 s64, 2
	s_cselect_b32 s64, 0, s64
	s_branch .Lfp_st_0
.Lfp_ipe:
	s_cmp_eq_u32 s44, 0
	s_cbranch_scc0 .Lfp_ipe_self
	s_mov_b32 s44, 1
	s_mov_b32 s46, 0
	s_mov_b32 s45, s39
	s_mov_b32 s47, s48
	v_cmp_gt_i32_e32 vcc, s48, v143
	s_nop 1
	v_cndmask_b32_e32 v147, v144, v149, vcc
	v_mov_b32_e32 v148, v150
	s_mov_b64 s[40:41], s[12:13]
	s_mov_b64 s[42:43], s[14:15]
	s_movk_i32 s49, 0x100
	s_mov_b32 s70, 0
	s_cmp_eq_u32 s51, 0
	s_cbranch_scc1 .Lfp_nx_0
	s_cmp_eq_u32 s51, 1
	s_cbranch_scc1 .Lfp_nx_1
	s_cmp_eq_u32 s51, 2
	s_cbranch_scc1 .Lfp_nx_2
	s_branch .Lfp_nx_3
.Lfp_ipe_self:
	s_mov_b32 s44, 2
	s_cmp_eq_u32 s51, 0
	s_cbranch_scc1 .Lfp_nx_0
	s_cmp_eq_u32 s51, 1
	s_cbranch_scc1 .Lfp_nx_1
	s_cmp_eq_u32 s51, 2
	s_cbranch_scc1 .Lfp_nx_2
	s_branch .Lfp_nx_3
.Lfp_iq:
	s_cmp_eq_u32 s46, 4
	s_cbranch_scc1 .Lfp_iq_use
	s_cmp_ge_u32 s46, 16
	s_cbranch_scc1 .Lfp_iq_fb
	s_lshl_b32 s52, s34, 10
	s_lshl_b32 s53, s46, 6
	s_add_u32 s52, s52, s53
	s_cmp_eq_u32 s44, 0
	s_cselect_b32 s53, 0, 0xc35000
	s_add_u32 s52, s52, s53
	v_add_u32_e32 v160, s52, v145
	global_load_dword v148, v160, s[16:17]
	s_waitcnt vmcnt(0)
	s_branch .Lfp_iq_use
.Lfp_iq_fb:
	s_lshl_b32 s52, s34, 6
	v_lshrrev_b32_e32 v160, 2, v159
	v_lshl_add_u32 v160, v160, 2, s52
	s_cmp_eq_u32 s44, 0
	s_cselect_b32 s54, s26, s28
	s_cselect_b32 s55, s27, s29
	global_load_dword v161, v160, s[54:55]
	global_load_dword v162, v160, s[54:55] offset:4
	s_waitcnt vmcnt(0)
	v_add3_u32 v161, v161, s46, v143
	v_cmp_lt_i32_e64 s[58:59], v161, v162
	v_lshlrev_b32_e32 v161, 2, v161
	global_load_dword v148, v161, s[24:25]
	s_waitcnt vmcnt(0)
	v_cndmask_b32_e64 v148, v144, v148, s[58:59]
.Lfp_iq_use:
	s_sub_i32 s52, s47, s46
	v_cmp_gt_i32_e32 vcc, s52, v143
	s_nop 1
	v_cndmask_b32_e32 v147, v144, v148, vcc
	s_cmp_eq_u32 s51, 0
	s_cbranch_scc1 .Lfp_nx_0
	s_cmp_eq_u32 s51, 1
	s_cbranch_scc1 .Lfp_nx_1
	s_cmp_eq_u32 s51, 2
	s_cbranch_scc1 .Lfp_nx_2
	s_branch .Lfp_nx_3
.Lfp_ien:
	s_mov_b32 s34, s35
	v_readlane_b32 s52, v155, 0
	v_readlane_b32 s53, v155, 1
	s_cmp_lt_u32 s34, s32
	s_cselect_b32 s47, s52, 0
	s_cselect_b32 s48, s53, 0
	s_max_u32 s38, s47, 2
	s_max_u32 s39, s48, 2
	v_cmp_gt_i32_e32 vcc, s47, v143
	s_nop 1
	v_cndmask_b32_e32 v147, v144, v151, vcc
	v_mov_b32_e32 v148, v152
	v_mov_b32_e32 v149, v153
	v_mov_b32_e32 v150, v154
	v_mov_b32_e32 v165, v164
	s_mov_b32 s44, 0
	s_mov_b32 s46, 0
	s_mov_b32 s45, s38
	s_mov_b64 s[40:41], s[8:9]
	s_mov_b64 s[42:43], s[10:11]
	s_movk_i32 s49, 0x100
	s_mov_b32 s70, 0
	v_mov_b32_e32 v160, 1
	v_mov_b32_e32 v161, 0x25e00
	s_mov_b64 s[58:59], exec
	s_mov_b64 exec, 1
	ds_add_rtn_u32 v160, v161, v160
	s_waitcnt lgkmcnt(0)
	v_readfirstlane_b32 s35, v160
	s_mov_b64 exec, s[58:59]
	s_lshl_b32 s52, s35, 10
	v_add_u32_e32 v160, s52, v145
	global_load_dword v151, v160, s[16:17]
	global_load_dword v152, v160, s[16:17] offset:256
	global_load_dword v153, v160, s[18:19]
	global_load_dword v154, v160, s[18:19] offset:256
	s_lshl_b32 s52, s35, 2
	v_and_b32_e32 v161, 1, v159
	v_mul_u32_u24_e32 v161, 0xc350, v161
	v_add_u32_e32 v161, s52, v161
	global_load_dword v155, v161, s[20:21]
	s_min_u32 s52, s35, 12499
	s_lshl_b32 s52, s52, 6
	v_lshl_add_u32 v161, v167, 2, s52
	global_load_dword v164, v161, s[30:31]
	s_cmp_eq_u32 s51, 0
	s_cbranch_scc1 .Lfp_nx_0
	s_cmp_eq_u32 s51, 1
	s_cbranch_scc1 .Lfp_nx_1
	s_cmp_eq_u32 s51, 2
	s_cbranch_scc1 .Lfp_nx_2
	s_branch .Lfp_nx_3
.Lfp_partend:
	ds_write_b128 v136, v[66:69]
	ds_write_b128 v136, v[70:73] offset:64
	ds_write_b128 v136, v[74:77] offset:128
	ds_write_b128 v136, v[78:81] offset:192
	s_cmp_eq_u32 s66, 0
	s_cbranch_scc0 .Lfp_pe1
	v_mov_b32_e32 v66, 0
	v_mov_b32_e32 v67, 0
	v_mov_b32_e32 v68, 0
	v_mov_b32_e32 v69, 0
	v_mov_b32_e32 v70, 0
	v_mov_b32_e32 v71, 0
	v_mov_b32_e32 v72, 0
	v_mov_b32_e32 v73, 0
	v_mov_b32_e32 v74, 0
	v_mov_b32_e32 v75, 0
	v_mov_b32_e32 v76, 0
	v_mov_b32_e32 v77, 0
	v_mov_b32_e32 v78, 0
	v_mov_b32_e32 v79, 0
	v_mov_b32_e32 v80, 0
	v_mov_b32_e32 v81, 0
	ds_read_b128 v[126:129], v137
	ds_read_b128 v[114:117], v138
	ds_read_b128 v[118:121], v138 offset:1024
	ds_read_b128 v[122:125], v138 offset:2048
	s_waitcnt lgkmcnt(2)
	v_mfma_f32_16x16x32_f16 v[82:85], v[126:129], v[114:117], v[82:85]
	ds_read_b128 v[114:117], v138 offset:3072
	s_waitcnt lgkmcnt(2)
	v_mfma_f32_16x16x32_f16 v[86:89], v[126:129], v[118:121], v[86:89]
	ds_read_b128 v[118:121], v138 offset:4096
	s_waitcnt lgkmcnt(2)
	v_mfma_f32_16x16x32_f16 v[90:93], v[126:129], v[122:125], v[90:93]
	ds_read_b128 v[122:125], v138 offset:5120
	s_waitcnt lgkmcnt(2)
	v_mfma_f32_16x16x32_f16 v[94:97], v[126:129], v[114:117], v[94:97]
	ds_read_b128 v[114:117], v138 offset:6144
	s_waitcnt lgkmcnt(2)
	v_mfma_f32_16x16x32_f16 v[98:101], v[126:129], v[118:121], v[98:101]
	ds_read_b128 v[118:121], v138 offset:7168
	s_waitcnt lgkmcnt(2)
	v_mfma_f32_16x16x32_f16 v[102:105], v[126:129], v[122:125], v[102:105]
	ds_read_b128 v[130:133], v137 offset:64
	ds_read_b128 v[122:125], v138 offset:8192
	s_waitcnt lgkmcnt(3)
	v_mfma_f32_16x16x32_f16 v[106:109], v[126:129], v[114:117], v[106:109]
	ds_read_b128 v[114:117], v138 offset:9216
	s_waitcnt lgkmcnt(3)
	v_mfma_f32_16x16x32_f16 v[110:113], v[126:129], v[118:121], v[110:113]
	ds_read_b128 v[118:121], v138 offset:10240
	s_waitcnt lgkmcnt(2)
	v_mfma_f32_16x16x32_f16 v[82:85], v[130:133], v[122:125], v[82:85]
	ds_read_b128 v[122:125], v138 offset:11264
	s_waitcnt lgkmcnt(2)
	v_mfma_f32_16x16x32_f16 v[86:89], v[130:133], v[114:117], v[86:89]
	ds_read_b128 v[114:117], v138 offset:12288
	s_waitcnt lgkmcnt(2)
	v_mfma_f32_16x16x32_f16 v[90:93], v[130:133], v[118:121], v[90:93]
	ds_read_b128 v[118:121], v138 offset:13312
	s_waitcnt lgkmcnt(2)
	v_mfma_f32_16x16x32_f16 v[94:97], v[130:133], v[122:125], v[94:97]
	ds_read_b128 v[122:125], v138 offset:14336
	s_waitcnt lgkmcnt(2)
	v_mfma_f32_16x16x32_f16 v[98:101], v[130:133], v[114:117], v[98:101]
	ds_read_b128 v[114:117], v138 offset:15360
	s_waitcnt lgkmcnt(2)
	v_mfma_f32_16x16x32_f16 v[102:105], v[130:133], v[118:121], v[102:105]
	ds_read_b128 v[126:129], v137 offset:128
	ds_read_b128 v[118:121], v138 offset:16384
	s_waitcnt lgkmcnt(3)
	v_mfma_f32_16x16x32_f16 v[106:109], v[130:133], v[122:125], v[106:109]
	ds_read_b128 v[122:125], v138 offset:17408
	s_waitcnt lgkmcnt(3)
	v_mfma_f32_16x16x32_f16 v[110:113], v[130:133], v[114:117], v[110:113]
	ds_read_b128 v[114:117], v138 offset:18432
	s_waitcnt lgkmcnt(2)
	v_mfma_f32_16x16x32_f16 v[82:85], v[126:129], v[118:121], v[82:85]
	ds_read_b128 v[118:121], v138 offset:19456
	s_waitcnt lgkmcnt(2)
	v_mfma_f32_16x16x32_f16 v[86:89], v[126:129], v[122:125], v[86:89]
	ds_read_b128 v[122:125], v138 offset:20480
	s_waitcnt lgkmcnt(2)
	v_mfma_f32_16x16x32_f16 v[90:93], v[126:129], v[114:117], v[90:93]
	ds_read_b128 v[114:117], v138 offset:21504
	s_waitcnt lgkmcnt(2)
	v_mfma_f32_16x16x32_f16 v[94:97], v[126:129], v[118:121], v[94:97]
	ds_read_b128 v[118:121], v138 offset:22528
	s_waitcnt lgkmcnt(2)
	v_mfma_f32_16x16x32_f16 v[98:101], v[126:129], v[122:125], v[98:101]
	ds_read_b128 v[122:125], v138 offset:23552
	s_waitcnt lgkmcnt(2)
	v_mfma_f32_16x16x32_f16 v[102:105], v[126:129], v[114:117], v[102:105]
	ds_read_b128 v[130:133], v137 offset:192
	ds_read_b128 v[114:117], v138 offset:24576
	s_waitcnt lgkmcnt(3)
	v_mfma_f32_16x16x32_f16 v[106:109], v[126:129], v[118:121], v[106:109]
	ds_read_b128 v[118:121], v138 offset:25600
	s_waitcnt lgkmcnt(3)
	v_mfma_f32_16x16x32_f16 v[110:113], v[126:129], v[122:125], v[110:113]
	ds_read_b128 v[122:125], v138 offset:26624
	s_waitcnt lgkmcnt(2)
	v_mfma_f32_16x16x32_f16 v[82:85], v[130:133], v[114:117], v[82:85]
	ds_read_b128 v[114:117], v138 offset:27648
	s_waitcnt lgkmcnt(2)
	v_mfma_f32_16x16x32_f16 v[86:89], v[130:133], v[118:121], v[86:89]
	ds_read_b128 v[118:121], v138 offset:28672
	s_waitcnt lgkmcnt(2)
	v_mfma_f32_16x16x32_f16 v[90:93], v[130:133], v[122:125], v[90:93]
	ds_read_b128 v[122:125], v138 offset:29696
	s_waitcnt lgkmcnt(2)
	v_mfma_f32_16x16x32_f16 v[94:97], v[130:133], v[114:117], v[94:97]
	ds_read_b128 v[114:117], v138 offset:30720
	s_waitcnt lgkmcnt(2)
	v_mfma_f32_16x16x32_f16 v[98:101], v[130:133], v[118:121], v[98:101]
	ds_read_b128 v[118:121], v138 offset:31744
	s_waitcnt lgkmcnt(2)
	v_mfma_f32_16x16x32_f16 v[102:105], v[130:133], v[122:125], v[102:105]
	s_waitcnt lgkmcnt(1)
	v_mfma_f32_16x16x32_f16 v[106:109], v[130:133], v[114:117], v[106:109]
	s_waitcnt lgkmcnt(0)
	v_mfma_f32_16x16x32_f16 v[110:113], v[130:133], v[118:121], v[110:113]
	s_mov_b32 s66, 1
	s_mov_b32 s65, s37
	s_cmp_eq_u32 s51, 0
	s_cbranch_scc1 .Lfp_is_0
	s_cmp_eq_u32 s51, 1
	s_cbranch_scc1 .Lfp_is_1
	s_cmp_eq_u32 s51, 2
	s_cbranch_scc1 .Lfp_is_2
	s_branch .Lfp_is_3
.Lfp_pe1:
	ds_read_b128 v[126:129], v137
	ds_read_b128 v[114:117], v138 offset:32768
	ds_read_b128 v[118:121], v138 offset:33792
	ds_read_b128 v[122:125], v138 offset:34816
	s_waitcnt lgkmcnt(2)
	v_mfma_f32_16x16x32_f16 v[82:85], v[126:129], v[114:117], v[82:85]
	ds_read_b128 v[114:117], v138 offset:35840
	s_waitcnt lgkmcnt(2)
	v_mfma_f32_16x16x32_f16 v[86:89], v[126:129], v[118:121], v[86:89]
	ds_read_b128 v[118:121], v138 offset:36864
	s_waitcnt lgkmcnt(2)
	v_mfma_f32_16x16x32_f16 v[90:93], v[126:129], v[122:125], v[90:93]
	ds_read_b128 v[122:125], v138 offset:37888
	s_waitcnt lgkmcnt(2)
	v_mfma_f32_16x16x32_f16 v[94:97], v[126:129], v[114:117], v[94:97]
	ds_read_b128 v[114:117], v138 offset:38912
	s_waitcnt lgkmcnt(2)
	v_mfma_f32_16x16x32_f16 v[98:101], v[126:129], v[118:121], v[98:101]
	ds_read_b128 v[118:121], v138 offset:39936
	s_waitcnt lgkmcnt(2)
	v_mfma_f32_16x16x32_f16 v[102:105], v[126:129], v[122:125], v[102:105]
	ds_read_b128 v[130:133], v137 offset:64
	ds_read_b128 v[122:125], v138 offset:40960
	s_waitcnt lgkmcnt(3)
	v_mfma_f32_16x16x32_f16 v[106:109], v[126:129], v[114:117], v[106:109]
	ds_read_b128 v[114:117], v138 offset:41984
	s_waitcnt lgkmcnt(3)
	v_mfma_f32_16x16x32_f16 v[110:113], v[126:129], v[118:121], v[110:113]
	ds_read_b128 v[118:121], v138 offset:43008
	s_waitcnt lgkmcnt(2)
	v_mfma_f32_16x16x32_f16 v[82:85], v[130:133], v[122:125], v[82:85]
	ds_read_b128 v[122:125], v138 offset:44032
	s_waitcnt lgkmcnt(2)
	v_mfma_f32_16x16x32_f16 v[86:89], v[130:133], v[114:117], v[86:89]
	ds_read_b128 v[114:117], v138 offset:45056
	s_waitcnt lgkmcnt(2)
	v_mfma_f32_16x16x32_f16 v[90:93], v[130:133], v[118:121], v[90:93]
	ds_read_b128 v[118:121], v138 offset:46080
	s_waitcnt lgkmcnt(2)
	v_mfma_f32_16x16x32_f16 v[94:97], v[130:133], v[122:125], v[94:97]
	ds_read_b128 v[122:125], v138 offset:47104
	s_waitcnt lgkmcnt(2)
	v_mfma_f32_16x16x32_f16 v[98:101], v[130:133], v[114:117], v[98:101]
	ds_read_b128 v[114:117], v138 offset:48128
	s_waitcnt lgkmcnt(2)
	v_mfma_f32_16x16x32_f16 v[102:105], v[130:133], v[118:121], v[102:105]
	ds_read_b128 v[126:129], v137 offset:128
	ds_read_b128 v[118:121], v138 offset:49152
	s_waitcnt lgkmcnt(3)
	v_mfma_f32_16x16x32_f16 v[106:109], v[130:133], v[122:125], v[106:109]
	ds_read_b128 v[122:125], v138 offset:50176
	s_waitcnt lgkmcnt(3)
	v_mfma_f32_16x16x32_f16 v[110:113], v[130:133], v[114:117], v[110:113]
	ds_read_b128 v[114:117], v138 offset:51200
	s_waitcnt lgkmcnt(2)
	v_mfma_f32_16x16x32_f16 v[82:85], v[126:129], v[118:121], v[82:85]
	ds_read_b128 v[118:121], v138 offset:52224
	s_waitcnt lgkmcnt(2)
	v_mfma_f32_16x16x32_f16 v[86:89], v[126:129], v[122:125], v[86:89]
	ds_read_b128 v[122:125], v138 offset:53248
	s_waitcnt lgkmcnt(2)
	v_mfma_f32_16x16x32_f16 v[90:93], v[126:129], v[114:117], v[90:93]
	ds_read_b128 v[114:117], v138 offset:54272
	s_waitcnt lgkmcnt(2)
	v_mfma_f32_16x16x32_f16 v[94:97], v[126:129], v[118:121], v[94:97]
	ds_read_b128 v[118:121], v138 offset:55296
	s_waitcnt lgkmcnt(2)
	v_mfma_f32_16x16x32_f16 v[98:101], v[126:129], v[122:125], v[98:101]
	ds_read_b128 v[122:125], v138 offset:56320
	s_waitcnt lgkmcnt(2)
	v_mfma_f32_16x16x32_f16 v[102:105], v[126:129], v[114:117], v[102:105]
	ds_read_b128 v[130:133], v137 offset:192
	ds_read_b128 v[114:117], v138 offset:57344
	s_waitcnt lgkmcnt(3)
	v_mfma_f32_16x16x32_f16 v[106:109], v[126:129], v[118:121], v[106:109]
	ds_read_b128 v[118:121], v138 offset:58368
	s_waitcnt lgkmcnt(3)
	v_mfma_f32_16x16x32_f16 v[110:113], v[126:129], v[122:125], v[110:113]
	ds_read_b128 v[122:125], v138 offset:59392
	s_waitcnt lgkmcnt(2)
	v_mfma_f32_16x16x32_f16 v[82:85], v[130:133], v[114:117], v[82:85]
	ds_read_b128 v[114:117], v138 offset:60416
	s_waitcnt lgkmcnt(2)
	v_mfma_f32_16x16x32_f16 v[86:89], v[130:133], v[118:121], v[86:89]
	ds_read_b128 v[118:121], v138 offset:61440
	s_waitcnt lgkmcnt(2)
	v_mfma_f32_16x16x32_f16 v[90:93], v[130:133], v[122:125], v[90:93]
	ds_read_b128 v[122:125], v138 offset:62464
	s_waitcnt lgkmcnt(2)
	v_mfma_f32_16x16x32_f16 v[94:97], v[130:133], v[114:117], v[94:97]
	ds_read_b128 v[114:117], v138 offset:63488
	s_waitcnt lgkmcnt(2)
	v_mfma_f32_16x16x32_f16 v[98:101], v[130:133], v[118:121], v[98:101]
	ds_read_b128 v[118:121], v138 offset:64512
	s_waitcnt lgkmcnt(2)
	v_mfma_f32_16x16x32_f16 v[102:105], v[130:133], v[122:125], v[102:105]
	s_waitcnt lgkmcnt(1)
	v_mfma_f32_16x16x32_f16 v[106:109], v[130:133], v[114:117], v[106:109]
	s_waitcnt lgkmcnt(0)
	v_mfma_f32_16x16x32_f16 v[110:113], v[130:133], v[118:121], v[110:113]
	s_mov_b32 s64, 1
	s_cmp_eq_u32 s51, 0
	s_cbranch_scc1 .Lfp_is_0
	s_cmp_eq_u32 s51, 1
	s_cbranch_scc1 .Lfp_is_1
	s_cmp_eq_u32 s51, 2
	s_cbranch_scc1 .Lfp_is_2
	s_branch .Lfp_is_3
.Lfp_tileend:
	ds_read_b128 v[126:129], v137
	ds_read_b128 v[114:117], v139
	ds_read_b128 v[118:121], v139 offset:1024
	ds_read_b128 v[122:125], v139 offset:2048
	s_waitcnt lgkmcnt(2)
	v_mfma_f32_16x16x32_f16 v[82:85], v[126:129], v[114:117], v[82:85]
	ds_read_b128 v[114:117], v139 offset:3072
	s_waitcnt lgkmcnt(2)
	v_mfma_f32_16x16x32_f16 v[86:89], v[126:129], v[118:121], v[86:89]
	ds_read_b128 v[118:121], v139 offset:4096
	s_waitcnt lgkmcnt(2)
	v_mfma_f32_16x16x32_f16 v[90:93], v[126:129], v[122:125], v[90:93]
	ds_read_b128 v[122:125], v139 offset:5120
	s_waitcnt lgkmcnt(2)
	v_mfma_f32_16x16x32_f16 v[94:97], v[126:129], v[114:117], v[94:97]
	ds_read_b128 v[114:117], v139 offset:6144
	s_waitcnt lgkmcnt(2)
	v_mfma_f32_16x16x32_f16 v[98:101], v[126:129], v[118:121], v[98:101]
	ds_read_b128 v[118:121], v139 offset:7168
	s_waitcnt lgkmcnt(2)
	v_mfma_f32_16x16x32_f16 v[102:105], v[126:129], v[122:125], v[102:105]
	ds_read_b128 v[130:133], v137 offset:64
	ds_read_b128 v[122:125], v139 offset:8192
	s_waitcnt lgkmcnt(3)
	v_mfma_f32_16x16x32_f16 v[106:109], v[126:129], v[114:117], v[106:109]
	ds_read_b128 v[114:117], v139 offset:9216
	s_waitcnt lgkmcnt(3)
	v_mfma_f32_16x16x32_f16 v[110:113], v[126:129], v[118:121], v[110:113]
	ds_read_b128 v[118:121], v139 offset:10240
	s_waitcnt lgkmcnt(2)
	v_mfma_f32_16x16x32_f16 v[82:85], v[130:133], v[122:125], v[82:85]
	ds_read_b128 v[122:125], v139 offset:11264
	s_waitcnt lgkmcnt(2)
	v_mfma_f32_16x16x32_f16 v[86:89], v[130:133], v[114:117], v[86:89]
	ds_read_b128 v[114:117], v139 offset:12288
	s_waitcnt lgkmcnt(2)
	v_mfma_f32_16x16x32_f16 v[90:93], v[130:133], v[118:121], v[90:93]
	ds_read_b128 v[118:121], v139 offset:13312
	s_waitcnt lgkmcnt(2)
	v_mfma_f32_16x16x32_f16 v[94:97], v[130:133], v[122:125], v[94:97]
	ds_read_b128 v[122:125], v139 offset:14336
	s_waitcnt lgkmcnt(2)
	v_mfma_f32_16x16x32_f16 v[98:101], v[130:133], v[114:117], v[98:101]
	ds_read_b128 v[114:117], v139 offset:15360
	s_waitcnt lgkmcnt(2)
	v_mfma_f32_16x16x32_f16 v[102:105], v[130:133], v[118:121], v[102:105]
	ds_read_b128 v[126:129], v137 offset:128
	ds_read_b128 v[118:121], v139 offset:16384
	s_waitcnt lgkmcnt(3)
	v_mfma_f32_16x16x32_f16 v[106:109], v[130:133], v[122:125], v[106:109]
	ds_read_b128 v[122:125], v139 offset:17408
	s_waitcnt lgkmcnt(3)
	v_mfma_f32_16x16x32_f16 v[110:113], v[130:133], v[114:117], v[110:113]
	ds_read_b128 v[114:117], v139 offset:18432
	s_waitcnt lgkmcnt(2)
	v_mfma_f32_16x16x32_f16 v[82:85], v[126:129], v[118:121], v[82:85]
	ds_read_b128 v[118:121], v139 offset:19456
	s_waitcnt lgkmcnt(2)
	v_mfma_f32_16x16x32_f16 v[86:89], v[126:129], v[122:125], v[86:89]
	ds_read_b128 v[122:125], v139 offset:20480
	s_waitcnt lgkmcnt(2)
	v_mfma_f32_16x16x32_f16 v[90:93], v[126:129], v[114:117], v[90:93]
	ds_read_b128 v[114:117], v139 offset:21504
	s_waitcnt lgkmcnt(2)
	v_mfma_f32_16x16x32_f16 v[94:97], v[126:129], v[118:121], v[94:97]
	ds_read_b128 v[118:121], v139 offset:22528
	s_waitcnt lgkmcnt(2)
	v_mfma_f32_16x16x32_f16 v[98:101], v[126:129], v[122:125], v[98:101]
	ds_read_b128 v[122:125], v139 offset:23552
	s_waitcnt lgkmcnt(2)
	v_mfma_f32_16x16x32_f16 v[102:105], v[126:129], v[114:117], v[102:105]
	ds_read_b128 v[130:133], v137 offset:192
	ds_read_b128 v[114:117], v139 offset:24576
	s_waitcnt lgkmcnt(3)
	v_mfma_f32_16x16x32_f16 v[106:109], v[126:129], v[118:121], v[106:109]
	ds_read_b128 v[118:121], v139 offset:25600
	s_waitcnt lgkmcnt(3)
	v_mfma_f32_16x16x32_f16 v[110:113], v[126:129], v[122:125], v[110:113]
	ds_read_b128 v[122:125], v139 offset:26624
	s_waitcnt lgkmcnt(2)
	v_mfma_f32_16x16x32_f16 v[82:85], v[130:133], v[114:117], v[82:85]
	ds_read_b128 v[114:117], v139 offset:27648
	s_waitcnt lgkmcnt(2)
	v_mfma_f32_16x16x32_f16 v[86:89], v[130:133], v[118:121], v[86:89]
	ds_read_b128 v[118:121], v139 offset:28672
	s_waitcnt lgkmcnt(2)
	v_mfma_f32_16x16x32_f16 v[90:93], v[130:133], v[122:125], v[90:93]
	ds_read_b128 v[122:125], v139 offset:29696
	s_waitcnt lgkmcnt(2)
	v_mfma_f32_16x16x32_f16 v[94:97], v[130:133], v[114:117], v[94:97]
	ds_read_b128 v[114:117], v139 offset:30720
	s_waitcnt lgkmcnt(2)
	v_mfma_f32_16x16x32_f16 v[98:101], v[130:133], v[118:121], v[98:101]
	ds_read_b128 v[118:121], v139 offset:31744
	s_waitcnt lgkmcnt(2)
	v_mfma_f32_16x16x32_f16 v[102:105], v[130:133], v[122:125], v[102:105]
	s_waitcnt lgkmcnt(1)
	v_mfma_f32_16x16x32_f16 v[106:109], v[130:133], v[114:117], v[106:109]
	s_waitcnt lgkmcnt(0)
	v_mfma_f32_16x16x32_f16 v[110:113], v[130:133], v[118:121], v[110:113]
	s_nop 7
	s_nop 3
	v_readlane_b32 s62, v166, 0
	v_readlane_b32 s63, v166, 15
	s_cmp_lg_u32 s62, s63
	s_cbranch_scc1 .Lfp_ep_nu
	v_max_f32_e32 v84, v84, v85
	v_max3_f32 v82, v82, v83, v84
	v_ashrrev_i32_e32 v83, 31, v82
	v_or_b32_e32 v83, 0x80000000, v83
	v_xor_b32_e32 v82, v82, v83
	v_max_f32_e32 v88, v88, v89
	v_max3_f32 v86, v86, v87, v88
	v_ashrrev_i32_e32 v87, 31, v86
	v_or_b32_e32 v87, 0x80000000, v87
	v_xor_b32_e32 v86, v86, v87
	v_max_f32_e32 v92, v92, v93
	v_max3_f32 v90, v90, v91, v92
	v_ashrrev_i32_e32 v91, 31, v90
	v_or_b32_e32 v91, 0x80000000, v91
	v_xor_b32_e32 v90, v90, v91
	v_max_f32_e32 v96, v96, v97
	v_max3_f32 v94, v94, v95, v96
	v_ashrrev_i32_e32 v95, 31, v94
	v_or_b32_e32 v95, 0x80000000, v95
	v_xor_b32_e32 v94, v94, v95
	v_max_f32_e32 v100, v100, v101
	v_max3_f32 v98, v98, v99, v100
	v_ashrrev_i32_e32 v99, 31, v98
	v_or_b32_e32 v99, 0x80000000, v99
	v_xor_b32_e32 v98, v98, v99
	v_max_f32_e32 v104, v104, v105
	v_max3_f32 v102, v102, v103, v104
	v_ashrrev_i32_e32 v103, 31, v102
	v_or_b32_e32 v103, 0x80000000, v103
	v_xor_b32_e32 v102, v102, v103
	v_max_f32_e32 v108, v108, v109
	v_max3_f32 v106, v106, v107, v108
	v_ashrrev_i32_e32 v107, 31, v106
	v_or_b32_e32 v107, 0x80000000, v107
	v_xor_b32_e32 v106, v106, v107
	v_max_f32_e32 v112, v112, v113
	v_max3_f32 v110, v110, v111, v112
	v_ashrrev_i32_e32 v111, 31, v110
	v_or_b32_e32 v111, 0x80000000, v111
	v_xor_b32_e32 v110, v110, v111
	s_sub_u32 s52, s62, s60
	s_cmp_lt_u32 s52, 8
	s_cbranch_scc0 .Lfp_ep_glob
	s_lshl_b32 s52, s52, 9
	s_add_u32 s52, s52, 0x24e00
	v_lshl_add_u32 v160, v167, 2, s52
	ds_max_u32 v160, v82
	ds_max_u32 v160, v86 offset:64
	ds_max_u32 v160, v90 offset:128
	ds_max_u32 v160, v94 offset:192
	ds_max_u32 v160, v98 offset:256
	ds_max_u32 v160, v102 offset:320
	ds_max_u32 v160, v106 offset:384
	ds_max_u32 v160, v110 offset:448
	s_branch .Lfp_ep_done
.Lfp_ep_glob:
	s_lshl_b32 s52, s62, 9
	v_lshl_add_u32 v160, v167, 2, s52
	global_atomic_umax v160, v82, s[22:23]
	global_atomic_umax v160, v86, s[22:23] offset:64
	global_atomic_umax v160, v90, s[22:23] offset:128
	global_atomic_umax v160, v94, s[22:23] offset:192
	global_atomic_umax v160, v98, s[22:23] offset:256
	global_atomic_umax v160, v102, s[22:23] offset:320
	global_atomic_umax v160, v106, s[22:23] offset:384
	global_atomic_umax v160, v110, s[22:23] offset:448
	s_branch .Lfp_ep_done
.Lfp_ep_nu:
	s_lshl_b32 s52, s33, 6
	v_lshrrev_b32_e32 v157, 4, v159
	v_lshl_add_u32 v157, v157, 4, s52
	global_load_dwordx4 v[160:163], v157, s[30:31]
	s_waitcnt vmcnt(0)
	v_lshlrev_b32_e32 v160, 9, v160
	v_lshl_add_u32 v160, v167, 2, v160
	v_lshlrev_b32_e32 v161, 9, v161
	v_lshl_add_u32 v161, v167, 2, v161
	v_lshlrev_b32_e32 v162, 9, v162
	v_lshl_add_u32 v162, v167, 2, v162
	v_lshlrev_b32_e32 v163, 9, v163
	v_lshl_add_u32 v163, v167, 2, v163
	v_ashrrev_i32_e32 v157, 31, v82
	v_or_b32_e32 v157, 0x80000000, v157
	v_xor_b32_e32 v82, v82, v157
	global_atomic_umax v160, v82, s[22:23]
	v_ashrrev_i32_e32 v157, 31, v83
	v_or_b32_e32 v157, 0x80000000, v157
	v_xor_b32_e32 v83, v83, v157
	global_atomic_umax v161, v83, s[22:23]
	v_ashrrev_i32_e32 v157, 31, v84
	v_or_b32_e32 v157, 0x80000000, v157
	v_xor_b32_e32 v84, v84, v157
	global_atomic_umax v162, v84, s[22:23]
	v_ashrrev_i32_e32 v157, 31, v85
	v_or_b32_e32 v157, 0x80000000, v157
	v_xor_b32_e32 v85, v85, v157
	global_atomic_umax v163, v85, s[22:23]
	v_ashrrev_i32_e32 v157, 31, v86
	v_or_b32_e32 v157, 0x80000000, v157
	v_xor_b32_e32 v86, v86, v157
	global_atomic_umax v160, v86, s[22:23] offset:64
	v_ashrrev_i32_e32 v157, 31, v87
	v_or_b32_e32 v157, 0x80000000, v157
	v_xor_b32_e32 v87, v87, v157
	global_atomic_umax v161, v87, s[22:23] offset:64
	v_ashrrev_i32_e32 v157, 31, v88
	v_or_b32_e32 v157, 0x80000000, v157
	v_xor_b32_e32 v88, v88, v157
	global_atomic_umax v162, v88, s[22:23] offset:64
	v_ashrrev_i32_e32 v157, 31, v89
	v_or_b32_e32 v157, 0x80000000, v157
	v_xor_b32_e32 v89, v89, v157
	global_atomic_umax v163, v89, s[22:23] offset:64
	v_ashrrev_i32_e32 v157, 31, v90
	v_or_b32_e32 v157, 0x80000000, v157
	v_xor_b32_e32 v90, v90, v157
	global_atomic_umax v160, v90, s[22:23] offset:128
	v_ashrrev_i32_e32 v157, 31, v91
	v_or_b32_e32 v157, 0x80000000, v157
	v_xor_b32_e32 v91, v91, v157
	global_atomic_umax v161, v91, s[22:23] offset:128
	v_ashrrev_i32_e32 v157, 31, v92
	v_or_b32_e32 v157, 0x80000000, v157
	v_xor_b32_e32 v92, v92, v157
	global_atomic_umax v162, v92, s[22:23] offset:128
	v_ashrrev_i32_e32 v157, 31, v93
	v_or_b32_e32 v157, 0x80000000, v157
	v_xor_b32_e32 v93, v93, v157
	global_atomic_umax v163, v93, s[22:23] offset:128
	v_ashrrev_i32_e32 v157, 31, v94
	v_or_b32_e32 v157, 0x80000000, v157
	v_xor_b32_e32 v94, v94, v157
	global_atomic_umax v160, v94, s[22:23] offset:192
	v_ashrrev_i32_e32 v157, 31, v95
	v_or_b32_e32 v157, 0x80000000, v157
	v_xor_b32_e32 v95, v95, v157
	global_atomic_umax v161, v95, s[22:23] offset:192
	v_ashrrev_i32_e32 v157, 31, v96
	v_or_b32_e32 v157, 0x80000000, v157
	v_xor_b32_e32 v96, v96, v157
	global_atomic_umax v162, v96, s[22:23] offset:192
	v_ashrrev_i32_e32 v157, 31, v97
	v_or_b32_e32 v157, 0x80000000, v157
	v_xor_b32_e32 v97, v97, v157
	global_atomic_umax v163, v97, s[22:23] offset:192
	v_ashrrev_i32_e32 v157, 31, v98
	v_or_b32_e32 v157, 0x80000000, v157
	v_xor_b32_e32 v98, v98, v157
	global_atomic_umax v160, v98, s[22:23] offset:256
	v_ashrrev_i32_e32 v157, 31, v99
	v_or_b32_e32 v157, 0x80000000, v157
	v_xor_b32_e32 v99, v99, v157
	global_atomic_umax v161, v99, s[22:23] offset:256
	v_ashrrev_i32_e32 v157, 31, v100
	v_or_b32_e32 v157, 0x80000000, v157
	v_xor_b32_e32 v100, v100, v157
	global_atomic_umax v162, v100, s[22:23] offset:256
	v_ashrrev_i32_e32 v157, 31, v101
	v_or_b32_e32 v157, 0x80000000, v157
	v_xor_b32_e32 v101, v101, v157
	global_atomic_umax v163, v101, s[22:23] offset:256
	v_ashrrev_i32_e32 v157, 31, v102
	v_or_b32_e32 v157, 0x80000000, v157
	v_xor_b32_e32 v102, v102, v157
	global_atomic_umax v160, v102, s[22:23] offset:320
	v_ashrrev_i32_e32 v157, 31, v103
	v_or_b32_e32 v157, 0x80000000, v157
	v_xor_b32_e32 v103, v103, v157
	global_atomic_umax v161, v103, s[22:23] offset:320
	v_ashrrev_i32_e32 v157, 31, v104
	v_or_b32_e32 v157, 0x80000000, v157
	v_xor_b32_e32 v104, v104, v157
	global_atomic_umax v162, v104, s[22:23] offset:320
	v_ashrrev_i32_e32 v157, 31, v105
	v_or_b32_e32 v157, 0x80000000, v157
	v_xor_b32_e32 v105, v105, v157
	global_atomic_umax v163, v105, s[22:23] offset:320
	v_ashrrev_i32_e32 v157, 31, v106
	v_or_b32_e32 v157, 0x80000000, v157
	v_xor_b32_e32 v106, v106, v157
	global_atomic_umax v160, v106, s[22:23] offset:384
	v_ashrrev_i32_e32 v157, 31, v107
	v_or_b32_e32 v157, 0x80000000, v157
	v_xor_b32_e32 v107, v107, v157
	global_atomic_umax v161, v107, s[22:23] offset:384
	v_ashrrev_i32_e32 v157, 31, v108
	v_or_b32_e32 v157, 0x80000000, v157
	v_xor_b32_e32 v108, v108, v157
	global_atomic_umax v162, v108, s[22:23] offset:384
	v_ashrrev_i32_e32 v157, 31, v109
	v_or_b32_e32 v157, 0x80000000, v157
	v_xor_b32_e32 v109, v109, v157
	global_atomic_umax v163, v109, s[22:23] offset:384
	v_ashrrev_i32_e32 v157, 31, v110
	v_or_b32_e32 v157, 0x80000000, v157
	v_xor_b32_e32 v110, v110, v157
	global_atomic_umax v160, v110, s[22:23] offset:448
	v_ashrrev_i32_e32 v157, 31, v111
	v_or_b32_e32 v157, 0x80000000, v157
	v_xor_b32_e32 v111, v111, v157
	global_atomic_umax v161, v111, s[22:23] offset:448
	v_ashrrev_i32_e32 v157, 31, v112
	v_or_b32_e32 v157, 0x80000000, v157
	v_xor_b32_e32 v112, v112, v157
	global_atomic_umax v162, v112, s[22:23] offset:448
	v_ashrrev_i32_e32 v157, 31, v113
	v_or_b32_e32 v157, 0x80000000, v157
	v_xor_b32_e32 v113, v113, v157
	global_atomic_umax v163, v113, s[22:23] offset:448
.Lfp_ep_done:
	s_mov_b32 s66, 0
	s_branch .Lfp_tilestart
.Lfp_exit:
	s_waitcnt vmcnt(0) lgkmcnt(0)
	s_barrier
	v_mov_b32_e32 v160, v0
	v_cmp_gt_u32_e32 vcc, 0x400, v160
	s_and_saveexec_b64 s[58:59], vcc
	s_cbranch_execz .Lfp_fl0
	v_lshlrev_b32_e32 v161, 2, v160
	v_add_u32_e32 v161, 0x24e00, v161
	ds_read_b32 v162, v161
	v_lshrrev_b32_e32 v163, 7, v160
	v_add_u32_e32 v163, s60, v163
	v_and_b32_e32 v161, 0x7f, v160
	v_lshl_add_u32 v161, v163, 7, v161
	v_lshlrev_b32_e32 v161, 2, v161
	v_cmp_gt_u32_e32 vcc, 0x100, v163
	s_and_b64 exec, exec, vcc
	s_waitcnt lgkmcnt(0)
	v_cmp_ne_u32_e32 vcc, 0, v162
	s_and_b64 exec, exec, vcc
	s_cbranch_execz .Lfp_fl0
	global_atomic_umax v161, v162, s[22:23]
.Lfp_fl0:
	s_mov_b64 exec, s[58:59]
	v_add_u32_e32 v160, 0x300, v0
	v_cmp_gt_u32_e32 vcc, 0x400, v160
	s_and_saveexec_b64 s[58:59], vcc
	s_cbranch_execz .Lfp_fl1
	v_lshlrev_b32_e32 v161, 2, v160
	v_add_u32_e32 v161, 0x24e00, v161
	ds_read_b32 v162, v161
	v_lshrrev_b32_e32 v163, 7, v160
	v_add_u32_e32 v163, s60, v163
	v_and_b32_e32 v161, 0x7f, v160
	v_lshl_add_u32 v161, v163, 7, v161
	v_lshlrev_b32_e32 v161, 2, v161
	v_cmp_gt_u32_e32 vcc, 0x100, v163
	s_and_b64 exec, exec, vcc
	s_waitcnt lgkmcnt(0)
	v_cmp_ne_u32_e32 vcc, 0, v162
	s_and_b64 exec, exec, vcc
	s_cbranch_execz .Lfp_fl1
	global_atomic_umax v161, v162, s[22:23]
.Lfp_fl1:
	s_mov_b64 exec, s[58:59]
	s_endpgm

	.amdhsa_kernel _Z12k_layer_pool9LayerArgs
		.amdhsa_group_segment_fixed_size 155140
		.amdhsa_private_segment_fixed_size 0
		.amdhsa_kernarg_size 360
		.amdhsa_user_sgpr_count 2
		.amdhsa_user_sgpr_dispatch_ptr 0
		.amdhsa_user_sgpr_queue_ptr 0
		.amdhsa_user_sgpr_kernarg_segment_ptr 1
		.amdhsa_user_sgpr_dispatch_id 0
		.amdhsa_user_sgpr_kernarg_preload_length 0
		.amdhsa_user_sgpr_kernarg_preload_offset 0
		.amdhsa_user_sgpr_private_segment_size 0
		.amdhsa_uses_dynamic_stack 0
		.amdhsa_enable_private_segment 0
		.amdhsa_system_sgpr_workgroup_id_x 1
		.amdhsa_system_sgpr_workgroup_id_y 0
		.amdhsa_system_sgpr_workgroup_id_z 0
		.amdhsa_system_sgpr_workgroup_info 0
		.amdhsa_system_vgpr_workitem_id 0
		.amdhsa_next_free_vgpr 168
		.amdhsa_next_free_sgpr 96
		.amdhsa_accum_offset 168
		.amdhsa_reserve_vcc 1
		.amdhsa_float_round_mode_32 0
		.amdhsa_float_round_mode_16_64 0
		.amdhsa_float_denorm_mode_32 3
		.amdhsa_float_denorm_mode_16_64 3
		.amdhsa_dx10_clamp 1
		.amdhsa_ieee_mode 1
		.amdhsa_fp16_overflow 0
		.amdhsa_tg_split 0
		.amdhsa_exception_fp_ieee_invalid_op 0
		.amdhsa_exception_fp_denorm_src 0
		.amdhsa_exception_fp_ieee_div_zero 0
		.amdhsa_exception_fp_ieee_overflow 0
		.amdhsa_exception_fp_ieee_underflow 0
		.amdhsa_exception_fp_ieee_inexact 0
		.amdhsa_exception_int_div_zero 0
	.end_amdhsa_kernel

	.text
	.protected	_Z10k_layer_fhILi96ELb1EEv9LayerArgsS0_i
	.globl	_Z10k_layer_fhILi96ELb1EEv9LayerArgsS0_i
	.p2align	8
	.type	_Z10k_layer_fhILi96ELb1EEv9LayerArgsS0_i,@function
_Z10k_layer_fhILi96ELb1EEv9LayerArgsS0_i:
	s_movk_i32 s3, 0x50
	v_lshrrev_b32_e32 v133, 6, v0
	s_movk_i32 s4, 0x1100
	v_mov_b32_e32 v1, 0x18000
	v_mad_u32_u24 v1, v133, s4, v1
	s_mov_b64 s[4:5], -1
	s_waitcnt lgkmcnt(0)
	s_cmp_ge_i32 s2, s3
	v_lshlrev_b32_e32 v130, 4, v0
	s_cbranch_scc0 .LBB5_73
	s_load_dwordx8 s[4:11], s[0:1], 0x0
	s_load_dwordx8 s[12:19], s[0:1], 0x20
	s_load_dwordx2 s[22:23], s[0:1], 0x40
	v_and_b32_e32 v159, 63, v0
	v_lshrrev_b32_e32 v160, 6, v0
	v_and_b32_e32 v143, 3, v159
	v_and_b32_e32 v167, 15, v159
	s_nop 0
	v_readfirstlane_b32 s61, v160
	s_waitcnt lgkmcnt(0)
	s_mov_b64 s[26:27], s[6:7]
	s_mov_b64 s[28:29], s[10:11]
	s_mov_b64 s[24:25], s[14:15]
	s_mov_b64 s[64:65], s[16:17]
	s_mov_b64 s[66:67], s[18:19]
	s_mov_b64 s[68:69], s[8:9]
	s_mov_b32 s8, s4
	s_and_b32 s9, s5, 0xffff
	s_mov_b32 s10, 0x40000000
	s_mov_b32 s11, 0x20000
	s_mov_b32 s12, s68
	s_and_b32 s13, s69, 0xffff
	s_mov_b32 s14, 0x40000000
	s_mov_b32 s15, 0x20000
	s_add_u32 s16, s24, 0x712bd00
	s_addc_u32 s17, s25, 0
	s_add_u32 s18, s16, 0xc35000
	s_addc_u32 s19, s17, 0
	s_add_u32 s20, s16, 0x186a000
	s_addc_u32 s21, s17, 0
	s_sub_u32 s52, s2, 80
	s_mul_i32 s52, s52, 72
	s_add_u32 s32, s52, 72
	s_min_u32 s32, s32, 12500
	s_mov_b32 s40, s64
	s_and_b32 s41, s65, 0xffff
	s_mov_b32 s42, 0x14000
	s_mov_b32 s43, 0x20000
	v_lshlrev_b32_e32 v160, 4, v0
	buffer_load_dwordx4 v[2:5], v160, s[40:43], 0 offen
	v_add_u32_e32 v161, 0x3000, v160
	buffer_load_dwordx4 v[6:9], v161, s[40:43], 0 offen
	v_add_u32_e32 v161, 0x6000, v160
	buffer_load_dwordx4 v[10:13], v161, s[40:43], 0 offen
	v_add_u32_e32 v161, 0x9000, v160
	buffer_load_dwordx4 v[14:17], v161, s[40:43], 0 offen
	v_add_u32_e32 v161, 0xc000, v160
	buffer_load_dwordx4 v[18:21], v161, s[40:43], 0 offen
	v_add_u32_e32 v161, 0xf000, v160
	buffer_load_dwordx4 v[22:25], v161, s[40:43], 0 offen
	v_add_u32_e32 v161, 0x12000, v160
	buffer_load_dwordx4 v[26:29], v161, s[40:43], 0 offen
	v_lshlrev_b32_e32 v162, 2, v0
	v_cmp_gt_u32_e32 vcc, 0x80, v0
	s_and_saveexec_b64 s[58:59], vcc
	s_cbranch_execz .Lfa_nobias
	global_load_dword v163, v162, s[66:67]
.Lfa_nobias:
	s_mov_b64 exec, s[58:59]
	s_waitcnt vmcnt(6)
	ds_write_b128 v160, v[2:5]
	s_waitcnt vmcnt(5)
	v_add_u32_e32 v161, 0x3000, v160
	ds_write_b128 v161, v[6:9]
	s_waitcnt vmcnt(4)
	v_add_u32_e32 v161, 0x6000, v160
	ds_write_b128 v161, v[10:13]
	s_waitcnt vmcnt(3)
	v_add_u32_e32 v161, 0x9000, v160
	ds_write_b128 v161, v[14:17]
	s_waitcnt vmcnt(2)
	v_add_u32_e32 v161, 0xc000, v160
	ds_write_b128 v161, v[18:21]
	s_waitcnt vmcnt(1)
	v_add_u32_e32 v161, 0xf000, v160
	ds_write_b128 v161, v[22:25]
	s_waitcnt vmcnt(0)
	v_add_u32_e32 v161, 0x12000, v160
	ds_write_b128 v161, v[26:29]
	s_waitcnt vmcnt(0)
	v_cmp_gt_u32_e32 vcc, 0x80, v0
	s_and_saveexec_b64 s[58:59], vcc
	v_add_u32_e32 v162, 0x24c00, v162
	ds_write_b32 v162, v163
	s_mov_b64 exec, s[58:59]
	v_cmp_eq_u32_e32 vcc, 0, v0
	s_and_saveexec_b64 s[58:59], vcc
	v_mov_b32_e32 v160, 0x24e00
	v_mov_b32_e32 v161, s52
	ds_write_b32 v160, v161
	s_mov_b64 exec, s[58:59]
	s_waitcnt lgkmcnt(0)
	s_barrier
	s_mul_i32 s61, s61, 0x1100
	s_add_u32 s61, s61, 0x18000
	v_lshrrev_b32_e32 v160, 2, v159
	v_lshrrev_b32_e32 v161, 4, v159
	v_lshlrev_b32_e32 v134, 4, v143
	v_mov_b32_e32 v135, v134
	v_mul_u32_u24_e32 v162, 0x110, v160
	v_add3_u32 v136, v162, v134, s61
	v_mul_u32_u24_e32 v162, 0x110, v167
	v_lshl_add_u32 v137, v161, 4, v162
	v_add_u32_e32 v137, s61, v137
	v_lshl_add_u32 v140, v161, 3, v162
	v_add_u32_e32 v140, s61, v140
	v_mul_u32_u24_e32 v162, 0x110, v161
	v_lshl_add_u32 v141, v167, 4, v162
	v_add_u32_e32 v141, s61, v141
	v_lshlrev_b32_e32 v138, 4, v159
	v_add_u32_e32 v139, 0x10000, v138
	v_lshlrev_b32_e32 v142, 8, v161
	v_lshl_add_u32 v142, v167, 4, v142
	v_mov_b32_e32 v144, 0x800000
	v_lshlrev_b32_e32 v145, 2, v160
	v_lshl_add_u32 v145, v143, 6, v145
	v_mul_u32_u24_e32 v146, 0xc0, v160
	v_add_u32_e32 v146, v146, v135
	v_mov_b32_e32 v160, 1
	v_mov_b32_e32 v161, 0x24e00
	s_mov_b64 s[58:59], exec
	s_mov_b64 exec, 1
	ds_add_rtn_u32 v160, v161, v160
	s_waitcnt lgkmcnt(0)
	v_readfirstlane_b32 s35, v160
	s_mov_b64 exec, s[58:59]
	s_lshl_b32 s52, s35, 10
	v_add_u32_e32 v160, s52, v145
	global_load_dword v151, v160, s[16:17]
	global_load_dword v152, v160, s[16:17] offset:256
	global_load_dword v153, v160, s[18:19]
	global_load_dword v154, v160, s[18:19] offset:256
	s_lshl_b32 s52, s35, 2
	v_and_b32_e32 v161, 1, v159
	v_mul_u32_u24_e32 v161, 0xc350, v161
	v_add_u32_e32 v161, s52, v161
	global_load_dword v155, v161, s[20:21]
	s_waitcnt vmcnt(0)
	s_mov_b32 s34, s35
	v_readlane_b32 s52, v155, 0
	v_readlane_b32 s53, v155, 1
	s_cmp_lt_u32 s34, s32
	s_cselect_b32 s47, s52, 0
	s_cselect_b32 s48, s53, 0
	s_max_u32 s38, s47, 2
	s_max_u32 s39, s48, 2
	v_cmp_gt_i32_e32 vcc, s47, v143
	s_nop 1
	v_cndmask_b32_e32 v147, v144, v151, vcc
	v_mov_b32_e32 v148, v152
	v_mov_b32_e32 v149, v153
	v_mov_b32_e32 v150, v154
	s_mov_b32 s44, 0
	s_mov_b32 s46, 0
	s_mov_b32 s45, s38
	s_mov_b64 s[40:41], s[8:9]
	s_mov_b64 s[42:43], s[10:11]
	s_movk_i32 s49, 0x100
	s_mov_b32 s70, 0
	v_mov_b32_e32 v160, 1
	v_mov_b32_e32 v161, 0x24e00
	s_mov_b64 s[58:59], exec
	s_mov_b64 exec, 1
	ds_add_rtn_u32 v160, v161, v160
	s_waitcnt lgkmcnt(0)
	v_readfirstlane_b32 s35, v160
	s_mov_b64 exec, s[58:59]
	s_lshl_b32 s52, s35, 10
	v_add_u32_e32 v160, s52, v145
	global_load_dword v151, v160, s[16:17]
	global_load_dword v152, v160, s[16:17] offset:256
	global_load_dword v153, v160, s[18:19]
	global_load_dword v154, v160, s[18:19] offset:256
	s_lshl_b32 s52, s35, 2
	v_and_b32_e32 v161, 1, v159
	v_mul_u32_u24_e32 v161, 0xc350, v161
	v_add_u32_e32 v161, s52, v161
	global_load_dword v155, v161, s[20:21]
	s_mov_b32 s64, 2
	s_mov_b32 s66, 0
.Lfa_tilestart:
	s_mov_b32 s33, s34
	s_mov_b32 s65, s38
	s_mov_b32 s37, s39
	s_cmp_ge_u32 s33, s32
	s_cbranch_scc1 .Lfa_exit
	v_mov_b32_e32 v66, 0
	v_mov_b32_e32 v67, 0
	v_mov_b32_e32 v68, 0
	v_mov_b32_e32 v69, 0
	v_mov_b32_e32 v70, 0
	v_mov_b32_e32 v71, 0
	v_mov_b32_e32 v72, 0
	v_mov_b32_e32 v73, 0
	v_mov_b32_e32 v74, 0
	v_mov_b32_e32 v75, 0
	v_mov_b32_e32 v76, 0
	v_mov_b32_e32 v77, 0
	v_mov_b32_e32 v78, 0
	v_mov_b32_e32 v79, 0
	v_mov_b32_e32 v80, 0
	v_mov_b32_e32 v81, 0
	v_lshrrev_b32_e32 v163, 4, v159
	v_lshlrev_b32_e32 v163, 4, v163
	v_add_u32_e32 v163, 0x24c00, v163
	ds_read_b128 v[82:85], v163 offset:0
	ds_read_b128 v[86:89], v163 offset:64
	ds_read_b128 v[90:93], v163 offset:128
	ds_read_b128 v[94:97], v163 offset:192
	ds_read_b128 v[98:101], v163 offset:256
	ds_read_b128 v[102:105], v163 offset:320
	ds_read_b128 v[106:109], v163 offset:384
	ds_read_b128 v[110:113], v163 offset:448
	s_waitcnt lgkmcnt(0)
	s_cmp_eq_u32 s64, 2
	s_cbranch_scc1 .Lfa_st_0
	s_mov_b32 s64, 0
	s_cmp_eq_u32 s51, 0
	s_cbranch_scc1 .Lfa_is_0
	s_cmp_eq_u32 s51, 1
	s_cbranch_scc1 .Lfa_is_1
	s_cmp_eq_u32 s51, 2
	s_cbranch_scc1 .Lfa_is_2
	s_branch .Lfa_is_3

.Lfa_iself_0:
	s_mul_i32 s52, s34, 0xc00
	v_add_u32_e32 v158, s52, v146
	v_or_b32_e32 v160, 0x80000000, v158
	buffer_load_dwordx4 v[2:5], v158, s[12:15], 0 offen
	buffer_load_dwordx4 v[6:9], v158, s[12:15], 0 offen offset:64
	buffer_load_dwordx4 v[10:13], v158, s[12:15], 0 offen offset:128
	buffer_load_dwordx4 v[14:17], v160, s[12:15], 0 offen offset:192
	s_mov_b32 s51, 0
	s_branch .Lfa_ien

.Lfa_iself_1:
	s_mul_i32 s52, s34, 0xc00
	v_add_u32_e32 v158, s52, v146
	v_or_b32_e32 v160, 0x80000000, v158
	buffer_load_dwordx4 v[18:21], v158, s[12:15], 0 offen
	buffer_load_dwordx4 v[22:25], v158, s[12:15], 0 offen offset:64
	buffer_load_dwordx4 v[26:29], v158, s[12:15], 0 offen offset:128
	buffer_load_dwordx4 v[30:33], v160, s[12:15], 0 offen offset:192
	s_mov_b32 s51, 1
	s_branch .Lfa_ien

.Lfa_iself_2:
	s_mul_i32 s52, s34, 0xc00
	v_add_u32_e32 v158, s52, v146
	v_or_b32_e32 v160, 0x80000000, v158
	buffer_load_dwordx4 v[34:37], v158, s[12:15], 0 offen
	buffer_load_dwordx4 v[38:41], v158, s[12:15], 0 offen offset:64
	buffer_load_dwordx4 v[42:45], v158, s[12:15], 0 offen offset:128
	buffer_load_dwordx4 v[46:49], v160, s[12:15], 0 offen offset:192
	s_mov_b32 s51, 2
	s_branch .Lfa_ien

.Lfa_iself_3:
	s_mul_i32 s52, s34, 0xc00
	v_add_u32_e32 v158, s52, v146
	v_or_b32_e32 v160, 0x80000000, v158
	buffer_load_dwordx4 v[50:53], v158, s[12:15], 0 offen
	buffer_load_dwordx4 v[54:57], v158, s[12:15], 0 offen offset:64
	buffer_load_dwordx4 v[58:61], v158, s[12:15], 0 offen offset:128
	buffer_load_dwordx4 v[62:65], v160, s[12:15], 0 offen offset:192
	s_mov_b32 s51, 3
	s_branch .Lfa_ien

.Lfa_ipe:
	s_cmp_eq_u32 s44, 0
	s_cbranch_scc0 .Lfa_ipe_self
	s_mov_b32 s44, 1
	s_mov_b32 s46, 0
	s_mov_b32 s45, s39
	s_mov_b32 s47, s48
	v_cmp_gt_i32_e32 vcc, s48, v143
	s_nop 1
	v_cndmask_b32_e32 v147, v144, v149, vcc
	v_mov_b32_e32 v148, v150
	s_mov_b64 s[40:41], s[12:13]
	s_mov_b64 s[42:43], s[14:15]
	s_movk_i32 s49, 0xc0
	s_mov_b32 s70, 0x80000000
	s_cmp_eq_u32 s51, 0
	s_cbranch_scc1 .Lfa_nx_0
	s_cmp_eq_u32 s51, 1
	s_cbranch_scc1 .Lfa_nx_1
	s_cmp_eq_u32 s51, 2
	s_cbranch_scc1 .Lfa_nx_2
	s_branch .Lfa_nx_3

.Lfa_ien:
	s_mov_b32 s34, s35
	v_readlane_b32 s52, v155, 0
	v_readlane_b32 s53, v155, 1
	s_cmp_lt_u32 s34, s32
	s_cselect_b32 s47, s52, 0
	s_cselect_b32 s48, s53, 0
	s_max_u32 s38, s47, 2
	s_max_u32 s39, s48, 2
	v_cmp_gt_i32_e32 vcc, s47, v143
	s_nop 1
	v_cndmask_b32_e32 v147, v144, v151, vcc
	v_mov_b32_e32 v148, v152
	v_mov_b32_e32 v149, v153
	v_mov_b32_e32 v150, v154
	s_mov_b32 s44, 0
	s_mov_b32 s46, 0
	s_mov_b32 s45, s38
	s_mov_b64 s[40:41], s[8:9]
	s_mov_b64 s[42:43], s[10:11]
	s_movk_i32 s49, 0x100
	s_mov_b32 s70, 0
	v_mov_b32_e32 v160, 1
	v_mov_b32_e32 v161, 0x24e00
	s_mov_b64 s[58:59], exec
	s_mov_b64 exec, 1
	ds_add_rtn_u32 v160, v161, v160
	s_waitcnt lgkmcnt(0)
	v_readfirstlane_b32 s35, v160
	s_mov_b64 exec, s[58:59]
	s_lshl_b32 s52, s35, 10
	v_add_u32_e32 v160, s52, v145
	global_load_dword v151, v160, s[16:17]
	global_load_dword v152, v160, s[16:17] offset:256
	global_load_dword v153, v160, s[18:19]
	global_load_dword v154, v160, s[18:19] offset:256
	s_lshl_b32 s52, s35, 2
	v_and_b32_e32 v161, 1, v159
	v_mul_u32_u24_e32 v161, 0xc350, v161
	v_add_u32_e32 v161, s52, v161
	global_load_dword v155, v161, s[20:21]
	s_cmp_eq_u32 s51, 0
	s_cbranch_scc1 .Lfa_nx_0
	s_cmp_eq_u32 s51, 1
	s_cbranch_scc1 .Lfa_nx_1
	s_cmp_eq_u32 s51, 2
	s_cbranch_scc1 .Lfa_nx_2
	s_branch .Lfa_nx_3
.Lfa_partend:
	ds_write_b128 v136, v[66:69]
	ds_write_b128 v136, v[70:73] offset:64
	ds_write_b128 v136, v[74:77] offset:128
	ds_write_b128 v136, v[78:81] offset:192
	s_cmp_eq_u32 s66, 0
	s_cbranch_scc0 .Lfa_pe1
	v_mov_b32_e32 v66, 0
	v_mov_b32_e32 v67, 0
	v_mov_b32_e32 v68, 0
	v_mov_b32_e32 v69, 0
	v_mov_b32_e32 v70, 0
	v_mov_b32_e32 v71, 0
	v_mov_b32_e32 v72, 0
	v_mov_b32_e32 v73, 0
	v_mov_b32_e32 v74, 0
	v_mov_b32_e32 v75, 0
	v_mov_b32_e32 v76, 0
	v_mov_b32_e32 v77, 0
	v_mov_b32_e32 v78, 0
	v_mov_b32_e32 v79, 0
	v_mov_b32_e32 v80, 0
	v_mov_b32_e32 v81, 0
	ds_read_b128 v[126:129], v137
	ds_read_b128 v[114:117], v138
	ds_read_b128 v[118:121], v138 offset:1024
	ds_read_b128 v[122:125], v138 offset:2048
	s_waitcnt lgkmcnt(2)
	v_mfma_f32_16x16x32_f16 v[82:85], v[114:117], v[126:129], v[82:85]
	ds_read_b128 v[114:117], v138 offset:3072
	s_waitcnt lgkmcnt(2)
	v_mfma_f32_16x16x32_f16 v[86:89], v[118:121], v[126:129], v[86:89]
	ds_read_b128 v[118:121], v138 offset:4096
	s_waitcnt lgkmcnt(2)
	v_mfma_f32_16x16x32_f16 v[90:93], v[122:125], v[126:129], v[90:93]
	ds_read_b128 v[122:125], v138 offset:5120
	s_waitcnt lgkmcnt(2)
	v_mfma_f32_16x16x32_f16 v[94:97], v[114:117], v[126:129], v[94:97]
	ds_read_b128 v[114:117], v138 offset:6144
	s_waitcnt lgkmcnt(2)
	v_mfma_f32_16x16x32_f16 v[98:101], v[118:121], v[126:129], v[98:101]
	ds_read_b128 v[118:121], v138 offset:7168
	s_waitcnt lgkmcnt(2)
	v_mfma_f32_16x16x32_f16 v[102:105], v[122:125], v[126:129], v[102:105]
	ds_read_b128 v[130:133], v137 offset:64
	ds_read_b128 v[122:125], v138 offset:8192
	s_waitcnt lgkmcnt(3)
	v_mfma_f32_16x16x32_f16 v[106:109], v[114:117], v[126:129], v[106:109]
	ds_read_b128 v[114:117], v138 offset:9216
	s_waitcnt lgkmcnt(3)
	v_mfma_f32_16x16x32_f16 v[110:113], v[118:121], v[126:129], v[110:113]
	ds_read_b128 v[118:121], v138 offset:10240
	s_waitcnt lgkmcnt(2)
	v_mfma_f32_16x16x32_f16 v[82:85], v[122:125], v[130:133], v[82:85]
	ds_read_b128 v[122:125], v138 offset:11264
	s_waitcnt lgkmcnt(2)
	v_mfma_f32_16x16x32_f16 v[86:89], v[114:117], v[130:133], v[86:89]
	ds_read_b128 v[114:117], v138 offset:12288
	s_waitcnt lgkmcnt(2)
	v_mfma_f32_16x16x32_f16 v[90:93], v[118:121], v[130:133], v[90:93]
	ds_read_b128 v[118:121], v138 offset:13312
	s_waitcnt lgkmcnt(2)
	v_mfma_f32_16x16x32_f16 v[94:97], v[122:125], v[130:133], v[94:97]
	ds_read_b128 v[122:125], v138 offset:14336
	s_waitcnt lgkmcnt(2)
	v_mfma_f32_16x16x32_f16 v[98:101], v[114:117], v[130:133], v[98:101]
	ds_read_b128 v[114:117], v138 offset:15360
	s_waitcnt lgkmcnt(2)
	v_mfma_f32_16x16x32_f16 v[102:105], v[118:121], v[130:133], v[102:105]
	ds_read_b128 v[126:129], v137 offset:128
	ds_read_b128 v[118:121], v138 offset:16384
	s_waitcnt lgkmcnt(3)
	v_mfma_f32_16x16x32_f16 v[106:109], v[122:125], v[130:133], v[106:109]
	ds_read_b128 v[122:125], v138 offset:17408
	s_waitcnt lgkmcnt(3)
	v_mfma_f32_16x16x32_f16 v[110:113], v[114:117], v[130:133], v[110:113]
	ds_read_b128 v[114:117], v138 offset:18432
	s_waitcnt lgkmcnt(2)
	v_mfma_f32_16x16x32_f16 v[82:85], v[118:121], v[126:129], v[82:85]
	ds_read_b128 v[118:121], v138 offset:19456
	s_waitcnt lgkmcnt(2)
	v_mfma_f32_16x16x32_f16 v[86:89], v[122:125], v[126:129], v[86:89]
	ds_read_b128 v[122:125], v138 offset:20480
	s_waitcnt lgkmcnt(2)
	v_mfma_f32_16x16x32_f16 v[90:93], v[114:117], v[126:129], v[90:93]
	ds_read_b128 v[114:117], v138 offset:21504
	s_waitcnt lgkmcnt(2)
	v_mfma_f32_16x16x32_f16 v[94:97], v[118:121], v[126:129], v[94:97]
	ds_read_b128 v[118:121], v138 offset:22528
	s_waitcnt lgkmcnt(2)
	v_mfma_f32_16x16x32_f16 v[98:101], v[122:125], v[126:129], v[98:101]
	ds_read_b128 v[122:125], v138 offset:23552
	s_waitcnt lgkmcnt(2)
	v_mfma_f32_16x16x32_f16 v[102:105], v[114:117], v[126:129], v[102:105]
	ds_read_b128 v[130:133], v137 offset:192
	ds_read_b128 v[114:117], v138 offset:24576
	s_waitcnt lgkmcnt(3)
	v_mfma_f32_16x16x32_f16 v[106:109], v[118:121], v[126:129], v[106:109]
	ds_read_b128 v[118:121], v138 offset:25600
	s_waitcnt lgkmcnt(3)
	v_mfma_f32_16x16x32_f16 v[110:113], v[122:125], v[126:129], v[110:113]
	ds_read_b128 v[122:125], v138 offset:26624
	s_waitcnt lgkmcnt(2)
	v_mfma_f32_16x16x32_f16 v[82:85], v[114:117], v[130:133], v[82:85]
	ds_read_b128 v[114:117], v138 offset:27648
	s_waitcnt lgkmcnt(2)
	v_mfma_f32_16x16x32_f16 v[86:89], v[118:121], v[130:133], v[86:89]
	ds_read_b128 v[118:121], v138 offset:28672
	s_waitcnt lgkmcnt(2)
	v_mfma_f32_16x16x32_f16 v[90:93], v[122:125], v[130:133], v[90:93]
	ds_read_b128 v[122:125], v138 offset:29696
	s_waitcnt lgkmcnt(2)
	v_mfma_f32_16x16x32_f16 v[94:97], v[114:117], v[130:133], v[94:97]
	ds_read_b128 v[114:117], v138 offset:30720
	s_waitcnt lgkmcnt(2)
	v_mfma_f32_16x16x32_f16 v[98:101], v[118:121], v[130:133], v[98:101]
	ds_read_b128 v[118:121], v138 offset:31744
	s_waitcnt lgkmcnt(2)
	v_mfma_f32_16x16x32_f16 v[102:105], v[122:125], v[130:133], v[102:105]
	s_waitcnt lgkmcnt(1)
	v_mfma_f32_16x16x32_f16 v[106:109], v[114:117], v[130:133], v[106:109]
	s_waitcnt lgkmcnt(0)
	v_mfma_f32_16x16x32_f16 v[110:113], v[118:121], v[130:133], v[110:113]
	s_mov_b32 s66, 1
	s_mov_b32 s65, s37
	s_cmp_eq_u32 s51, 0
	s_cbranch_scc1 .Lfa_is_0
	s_cmp_eq_u32 s51, 1
	s_cbranch_scc1 .Lfa_is_1
	s_cmp_eq_u32 s51, 2
	s_cbranch_scc1 .Lfa_is_2
	s_branch .Lfa_is_3
.Lfa_pe1:
	ds_read_b128 v[126:129], v137
	ds_read_b128 v[114:117], v138 offset:32768
	ds_read_b128 v[118:121], v138 offset:33792
	ds_read_b128 v[122:125], v138 offset:34816
	s_waitcnt lgkmcnt(2)
	v_mfma_f32_16x16x32_f16 v[82:85], v[114:117], v[126:129], v[82:85]
	ds_read_b128 v[114:117], v138 offset:35840
	s_waitcnt lgkmcnt(2)
	v_mfma_f32_16x16x32_f16 v[86:89], v[118:121], v[126:129], v[86:89]
	ds_read_b128 v[118:121], v138 offset:36864
	s_waitcnt lgkmcnt(2)
	v_mfma_f32_16x16x32_f16 v[90:93], v[122:125], v[126:129], v[90:93]
	ds_read_b128 v[122:125], v138 offset:37888
	s_waitcnt lgkmcnt(2)
	v_mfma_f32_16x16x32_f16 v[94:97], v[114:117], v[126:129], v[94:97]
	ds_read_b128 v[114:117], v138 offset:38912
	s_waitcnt lgkmcnt(2)
	v_mfma_f32_16x16x32_f16 v[98:101], v[118:121], v[126:129], v[98:101]
	ds_read_b128 v[118:121], v138 offset:39936
	s_waitcnt lgkmcnt(2)
	v_mfma_f32_16x16x32_f16 v[102:105], v[122:125], v[126:129], v[102:105]
	ds_read_b128 v[130:133], v137 offset:64
	ds_read_b128 v[122:125], v138 offset:40960
	s_waitcnt lgkmcnt(3)
	v_mfma_f32_16x16x32_f16 v[106:109], v[114:117], v[126:129], v[106:109]
	ds_read_b128 v[114:117], v138 offset:41984
	s_waitcnt lgkmcnt(3)
	v_mfma_f32_16x16x32_f16 v[110:113], v[118:121], v[126:129], v[110:113]
	ds_read_b128 v[118:121], v138 offset:43008
	s_waitcnt lgkmcnt(2)
	v_mfma_f32_16x16x32_f16 v[82:85], v[122:125], v[130:133], v[82:85]
	ds_read_b128 v[122:125], v138 offset:44032
	s_waitcnt lgkmcnt(2)
	v_mfma_f32_16x16x32_f16 v[86:89], v[114:117], v[130:133], v[86:89]
	ds_read_b128 v[114:117], v138 offset:45056
	s_waitcnt lgkmcnt(2)
	v_mfma_f32_16x16x32_f16 v[90:93], v[118:121], v[130:133], v[90:93]
	ds_read_b128 v[118:121], v138 offset:46080
	s_waitcnt lgkmcnt(2)
	v_mfma_f32_16x16x32_f16 v[94:97], v[122:125], v[130:133], v[94:97]
	ds_read_b128 v[122:125], v138 offset:47104
	s_waitcnt lgkmcnt(2)
	v_mfma_f32_16x16x32_f16 v[98:101], v[114:117], v[130:133], v[98:101]
	ds_read_b128 v[114:117], v138 offset:48128
	s_waitcnt lgkmcnt(2)
	v_mfma_f32_16x16x32_f16 v[102:105], v[118:121], v[130:133], v[102:105]
	ds_read_b128 v[126:129], v137 offset:128
	ds_read_b128 v[118:121], v138 offset:49152
	s_waitcnt lgkmcnt(3)
	v_mfma_f32_16x16x32_f16 v[106:109], v[122:125], v[130:133], v[106:109]
	ds_read_b128 v[122:125], v138 offset:50176
	s_waitcnt lgkmcnt(3)
	v_mfma_f32_16x16x32_f16 v[110:113], v[114:117], v[130:133], v[110:113]
	ds_read_b128 v[114:117], v138 offset:51200
	s_waitcnt lgkmcnt(2)
	v_mfma_f32_16x16x32_f16 v[82:85], v[118:121], v[126:129], v[82:85]
	ds_read_b128 v[118:121], v138 offset:52224
	s_waitcnt lgkmcnt(2)
	v_mfma_f32_16x16x32_f16 v[86:89], v[122:125], v[126:129], v[86:89]
	ds_read_b128 v[122:125], v138 offset:53248
	s_waitcnt lgkmcnt(2)
	v_mfma_f32_16x16x32_f16 v[90:93], v[114:117], v[126:129], v[90:93]
	ds_read_b128 v[114:117], v138 offset:54272
	s_waitcnt lgkmcnt(2)
	v_mfma_f32_16x16x32_f16 v[94:97], v[118:121], v[126:129], v[94:97]
	ds_read_b128 v[118:121], v138 offset:55296
	s_waitcnt lgkmcnt(2)
	v_mfma_f32_16x16x32_f16 v[98:101], v[122:125], v[126:129], v[98:101]
	ds_read_b128 v[122:125], v138 offset:56320
	s_waitcnt lgkmcnt(2)
	v_mfma_f32_16x16x32_f16 v[102:105], v[114:117], v[126:129], v[102:105]
	s_waitcnt lgkmcnt(1)
	v_mfma_f32_16x16x32_f16 v[106:109], v[118:121], v[126:129], v[106:109]
	s_waitcnt lgkmcnt(0)
	v_mfma_f32_16x16x32_f16 v[110:113], v[122:125], v[126:129], v[110:113]
	s_mov_b32 s64, 1
	s_cmp_eq_u32 s51, 0
	s_cbranch_scc1 .Lfa_is_0
	s_cmp_eq_u32 s51, 1
	s_cbranch_scc1 .Lfa_is_1
	s_cmp_eq_u32 s51, 2
	s_cbranch_scc1 .Lfa_is_2
	s_branch .Lfa_is_3
.Lfa_tileend:
	ds_read_b128 v[126:129], v137
	ds_read_b128 v[114:117], v138 offset:57344
	ds_read_b128 v[118:121], v138 offset:58368
	ds_read_b128 v[122:125], v138 offset:59392
	s_waitcnt lgkmcnt(2)
	v_mfma_f32_16x16x32_f16 v[82:85], v[114:117], v[126:129], v[82:85]
	ds_read_b128 v[114:117], v138 offset:60416
	s_waitcnt lgkmcnt(2)
	v_mfma_f32_16x16x32_f16 v[86:89], v[118:121], v[126:129], v[86:89]
	ds_read_b128 v[118:121], v138 offset:61440
	s_waitcnt lgkmcnt(2)
	v_mfma_f32_16x16x32_f16 v[90:93], v[122:125], v[126:129], v[90:93]
	ds_read_b128 v[122:125], v138 offset:62464
	s_waitcnt lgkmcnt(2)
	v_mfma_f32_16x16x32_f16 v[94:97], v[114:117], v[126:129], v[94:97]
	ds_read_b128 v[114:117], v138 offset:63488
	s_waitcnt lgkmcnt(2)
	v_mfma_f32_16x16x32_f16 v[98:101], v[118:121], v[126:129], v[98:101]
	ds_read_b128 v[118:121], v138 offset:64512
	s_waitcnt lgkmcnt(2)
	v_mfma_f32_16x16x32_f16 v[102:105], v[122:125], v[126:129], v[102:105]
	ds_read_b128 v[130:133], v137 offset:64
	ds_read_b128 v[122:125], v139
	s_waitcnt lgkmcnt(3)
	v_mfma_f32_16x16x32_f16 v[106:109], v[114:117], v[126:129], v[106:109]
	ds_read_b128 v[114:117], v139 offset:1024
	s_waitcnt lgkmcnt(3)
	v_mfma_f32_16x16x32_f16 v[110:113], v[118:121], v[126:129], v[110:113]
	ds_read_b128 v[118:121], v139 offset:2048
	s_waitcnt lgkmcnt(2)
	v_mfma_f32_16x16x32_f16 v[82:85], v[122:125], v[130:133], v[82:85]
	ds_read_b128 v[122:125], v139 offset:3072
	s_waitcnt lgkmcnt(2)
	v_mfma_f32_16x16x32_f16 v[86:89], v[114:117], v[130:133], v[86:89]
	ds_read_b128 v[114:117], v139 offset:4096
	s_waitcnt lgkmcnt(2)
	v_mfma_f32_16x16x32_f16 v[90:93], v[118:121], v[130:133], v[90:93]
	ds_read_b128 v[118:121], v139 offset:5120
	s_waitcnt lgkmcnt(2)
	v_mfma_f32_16x16x32_f16 v[94:97], v[122:125], v[130:133], v[94:97]
	ds_read_b128 v[122:125], v139 offset:6144
	s_waitcnt lgkmcnt(2)
	v_mfma_f32_16x16x32_f16 v[98:101], v[114:117], v[130:133], v[98:101]
	ds_read_b128 v[114:117], v139 offset:7168
	s_waitcnt lgkmcnt(2)
	v_mfma_f32_16x16x32_f16 v[102:105], v[118:121], v[130:133], v[102:105]
	ds_read_b128 v[126:129], v137 offset:128
	ds_read_b128 v[118:121], v139 offset:8192
	s_waitcnt lgkmcnt(3)
	v_mfma_f32_16x16x32_f16 v[106:109], v[122:125], v[130:133], v[106:109]
	ds_read_b128 v[122:125], v139 offset:9216
	s_waitcnt lgkmcnt(3)
	v_mfma_f32_16x16x32_f16 v[110:113], v[114:117], v[130:133], v[110:113]
	ds_read_b128 v[114:117], v139 offset:10240
	s_waitcnt lgkmcnt(2)
	v_mfma_f32_16x16x32_f16 v[82:85], v[118:121], v[126:129], v[82:85]
	ds_read_b128 v[118:121], v139 offset:11264
	s_waitcnt lgkmcnt(2)
	v_mfma_f32_16x16x32_f16 v[86:89], v[122:125], v[126:129], v[86:89]
	ds_read_b128 v[122:125], v139 offset:12288
	s_waitcnt lgkmcnt(2)
	v_mfma_f32_16x16x32_f16 v[90:93], v[114:117], v[126:129], v[90:93]
	ds_read_b128 v[114:117], v139 offset:13312
	s_waitcnt lgkmcnt(2)
	v_mfma_f32_16x16x32_f16 v[94:97], v[118:121], v[126:129], v[94:97]
	ds_read_b128 v[118:121], v139 offset:14336
	s_waitcnt lgkmcnt(2)
	v_mfma_f32_16x16x32_f16 v[98:101], v[122:125], v[126:129], v[98:101]
	ds_read_b128 v[122:125], v139 offset:15360
	s_waitcnt lgkmcnt(2)
	v_mfma_f32_16x16x32_f16 v[102:105], v[114:117], v[126:129], v[102:105]
	s_waitcnt lgkmcnt(1)
	v_mfma_f32_16x16x32_f16 v[106:109], v[118:121], v[126:129], v[106:109]
	s_waitcnt lgkmcnt(0)
	v_mfma_f32_16x16x32_f16 v[110:113], v[122:125], v[126:129], v[110:113]
	s_nop 7
	s_nop 3
	v_max_f32_e32 v82, 0, v82
	v_max_f32_e32 v83, 0, v83
	v_max_f32_e32 v84, 0, v84
	v_max_f32_e32 v85, 0, v85
	v_cvt_pk_f16_f32 v160, v82, v83
	v_cvt_pk_f16_f32 v161, v84, v85
	ds_write_b64 v140, v[160:161]
	v_max_f32_e32 v86, 0, v86
	v_max_f32_e32 v87, 0, v87
	v_max_f32_e32 v88, 0, v88
	v_max_f32_e32 v89, 0, v89
	v_cvt_pk_f16_f32 v162, v86, v87
	v_cvt_pk_f16_f32 v163, v88, v89
	ds_write_b64 v140, v[162:163] offset:32
	v_max_f32_e32 v90, 0, v90
	v_max_f32_e32 v91, 0, v91
	v_max_f32_e32 v92, 0, v92
	v_max_f32_e32 v93, 0, v93
	v_cvt_pk_f16_f32 v160, v90, v91
	v_cvt_pk_f16_f32 v161, v92, v93
	ds_write_b64 v140, v[160:161] offset:64
	v_max_f32_e32 v94, 0, v94
	v_max_f32_e32 v95, 0, v95
	v_max_f32_e32 v96, 0, v96
	v_max_f32_e32 v97, 0, v97
	v_cvt_pk_f16_f32 v162, v94, v95
	v_cvt_pk_f16_f32 v163, v96, v97
	ds_write_b64 v140, v[162:163] offset:96
	v_max_f32_e32 v98, 0, v98
	v_max_f32_e32 v99, 0, v99
	v_max_f32_e32 v100, 0, v100
	v_max_f32_e32 v101, 0, v101
	v_cvt_pk_f16_f32 v160, v98, v99
	v_cvt_pk_f16_f32 v161, v100, v101
	ds_write_b64 v140, v[160:161] offset:128
	v_max_f32_e32 v102, 0, v102
	v_max_f32_e32 v103, 0, v103
	v_max_f32_e32 v104, 0, v104
	v_max_f32_e32 v105, 0, v105
	v_cvt_pk_f16_f32 v162, v102, v103
	v_cvt_pk_f16_f32 v163, v104, v105
	ds_write_b64 v140, v[162:163] offset:160
	v_max_f32_e32 v106, 0, v106
	v_max_f32_e32 v107, 0, v107
	v_max_f32_e32 v108, 0, v108
	v_max_f32_e32 v109, 0, v109
	v_cvt_pk_f16_f32 v160, v106, v107
	v_cvt_pk_f16_f32 v161, v108, v109
	ds_write_b64 v140, v[160:161] offset:192
	v_max_f32_e32 v110, 0, v110
	v_max_f32_e32 v111, 0, v111
	v_max_f32_e32 v112, 0, v112
	v_max_f32_e32 v113, 0, v113
	v_cvt_pk_f16_f32 v162, v110, v111
	v_cvt_pk_f16_f32 v163, v112, v113
	ds_write_b64 v140, v[162:163] offset:224
	s_lshl_b32 s52, s33, 12
	v_add_u32_e32 v158, s52, v142
	ds_read_b128 v[114:117], v141
	ds_read_b128 v[118:121], v141 offset:1088
	ds_read_b128 v[122:125], v141 offset:2176
	ds_read_b128 v[126:129], v141 offset:3264
	s_waitcnt lgkmcnt(3)
	global_store_dwordx4 v158, v[114:117], s[22:23] sc1
	s_waitcnt lgkmcnt(2)
	global_store_dwordx4 v158, v[118:121], s[22:23] offset:1024 sc1
	s_waitcnt lgkmcnt(1)
	global_store_dwordx4 v158, v[122:125], s[22:23] offset:2048 sc1
	s_waitcnt lgkmcnt(0)
	global_store_dwordx4 v158, v[126:129], s[22:23] offset:3072 sc1
	s_nop 1
	s_mov_b32 s66, 0
	s_branch .Lfa_tilestart
.Lfa_exit:
	s_endpgm
.LBB5_73:
	s_and_b64 vcc, exec, s[4:5]
	s_cbranch_vccz .LBB5_129
	s_load_dwordx2 s[4:5], s[0:1], 0x98
	s_load_dword s10, s[0:1], 0xb4
	v_mov_b32_e32 v131, 0
	s_movk_i32 s6, 0x3000
	s_abs_i32 s8, s3
	s_waitcnt vmcnt(1) lgkmcnt(0)
	v_lshl_add_u64 v[10:11], s[4:5], 0, v[130:131]
	v_add_co_u32_e32 v12, vcc, s6, v10
	s_movk_i32 s6, 0x6000
	s_nop 0
	v_addc_co_u32_e32 v13, vcc, 0, v11, vcc
	s_waitcnt vmcnt(0)
	v_add_co_u32_e32 v14, vcc, s6, v10
	s_mov_b32 s6, 0x9000
	s_nop 0
	v_addc_co_u32_e32 v15, vcc, 0, v11, vcc
	v_add_co_u32_e32 v18, vcc, s6, v10
	global_load_dwordx4 v[6:9], v[12:13], off
	global_load_dwordx4 v[2:5], v[14:15], off
	v_addc_co_u32_e32 v19, vcc, 0, v11, vcc
	global_load_dwordx4 v[14:17], v130, s[4:5]
	global_load_dwordx4 v[10:13], v[18:19], off
	v_cvt_f32_u32_e32 v18, s8
	s_sub_i32 s6, 0, s8
	s_add_i32 s11, s3, s10
	s_add_i32 s11, s11, -1
	v_rcp_iflag_f32_e32 v18, v18
	s_abs_i32 s9, s11
	v_mov_b32_e32 v19, v131
	v_mov_b32_e32 v20, v131
	v_mul_f32_e32 v18, 0x4f7ffffe, v18
	v_cvt_u32_f32_e32 v18, v18
	v_mov_b32_e32 v21, v131
	v_readfirstlane_b32 s12, v18
	s_mul_i32 s6, s6, s12
	s_mul_hi_u32 s6, s12, s6
	s_add_i32 s12, s12, s6
	v_or_b32_e32 v18, 0xc00, v0
	s_movk_i32 s6, 0xe00
	v_cmp_gt_u32_e32 vcc, s6, v18
	s_and_saveexec_b64 s[6:7], vcc
	s_cbranch_execz .LBB5_76
	v_lshlrev_b32_e32 v18, 4, v18
	global_load_dwordx4 v[18:21], v18, s[4:5]
	s_waitcnt vmcnt(0)
	v_mov_b32_e32 v131, v18

	.amdhsa_kernel _Z10k_layer_fhILi96ELb1EEv9LayerArgsS0_i
		.amdhsa_group_segment_fixed_size 151044
		.amdhsa_private_segment_fixed_size 0
		.amdhsa_kernarg_size 472
		.amdhsa_user_sgpr_count 2
		.amdhsa_user_sgpr_dispatch_ptr 0
		.amdhsa_user_sgpr_queue_ptr 0
		.amdhsa_user_sgpr_kernarg_segment_ptr 1
		.amdhsa_user_sgpr_dispatch_id 0
		.amdhsa_user_sgpr_kernarg_preload_length 0
		.amdhsa_user_sgpr_kernarg_preload_offset 0
		.amdhsa_user_sgpr_private_segment_size 0
		.amdhsa_uses_dynamic_stack 0
		.amdhsa_enable_private_segment 0
		.amdhsa_system_sgpr_workgroup_id_x 1
		.amdhsa_system_sgpr_workgroup_id_y 0
		.amdhsa_system_sgpr_workgroup_id_z 0
		.amdhsa_system_sgpr_workgroup_info 0
		.amdhsa_system_vgpr_workitem_id 0
		.amdhsa_next_free_vgpr 168
		.amdhsa_next_free_sgpr 96
		.amdhsa_accum_offset 168
		.amdhsa_reserve_vcc 1
		.amdhsa_float_round_mode_32 0
		.amdhsa_float_round_mode_16_64 0
		.amdhsa_float_denorm_mode_32 3
		.amdhsa_float_denorm_mode_16_64 3
		.amdhsa_dx10_clamp 1
		.amdhsa_ieee_mode 1
		.amdhsa_fp16_overflow 0
		.amdhsa_tg_split 0
		.amdhsa_exception_fp_ieee_invalid_op 0
		.amdhsa_exception_fp_denorm_src 0
		.amdhsa_exception_fp_ieee_div_zero 0
		.amdhsa_exception_fp_ieee_overflow 0
		.amdhsa_exception_fp_ieee_underflow 0
		.amdhsa_exception_fp_ieee_inexact 0
		.amdhsa_exception_int_div_zero 0
	.end_amdhsa_kernel
	.text
.Lfunc_end5:
	.size	_Z10k_layer_fhILi96ELb1EEv9LayerArgsS0_i, .Lfunc_end5-_Z10k_layer_fhILi96ELb1EEv9LayerArgsS0_i
	.set _Z10k_layer_fhILi96ELb1EEv9LayerArgsS0_i.num_vgpr, 166
	.set _Z10k_layer_fhILi96ELb1EEv9LayerArgsS0_i.num_agpr, 0
	.set _Z10k_layer_fhILi96ELb1EEv9LayerArgsS0_i.numbered_sgpr, 46
	.set _Z10k_layer_fhILi96ELb1EEv9LayerArgsS0_i.num_named_barrier, 0
	.set _Z10k_layer_fhILi96ELb1EEv9LayerArgsS0_i.private_seg_size, 0
	.set _Z10k_layer_fhILi96ELb1EEv9LayerArgsS0_i.uses_vcc, 1
	.set _Z10k_layer_fhILi96ELb1EEv9LayerArgsS0_i.uses_flat_scratch, 0
	.set _Z10k_layer_fhILi96ELb1EEv9LayerArgsS0_i.has_dyn_sized_stack, 0
	.set _Z10k_layer_fhILi96ELb1EEv9LayerArgsS0_i.has_recursion, 0
	.set _Z10k_layer_fhILi96ELb1EEv9LayerArgsS0_i.has_indirect_call, 0

	.text
	.protected	_Z10k_layer_fhILi128ELb1EEv9LayerArgsS0_i
	.globl	_Z10k_layer_fhILi128ELb1EEv9LayerArgsS0_i
	.p2align	8
	.type	_Z10k_layer_fhILi128ELb1EEv9LayerArgsS0_i,@function
_Z10k_layer_fhILi128ELb1EEv9LayerArgsS0_i:
	s_movk_i32 s3, 0x50
	v_lshrrev_b32_e32 v138, 6, v0
	s_movk_i32 s4, 0x1100
	v_mov_b32_e32 v1, 0x18000
	v_mad_u32_u24 v1, v138, s4, v1
	s_mov_b64 s[4:5], -1
	s_waitcnt lgkmcnt(0)
	s_cmp_ge_i32 s2, s3
	v_lshlrev_b32_e32 v130, 4, v0
	s_cbranch_scc0 .LBB6_69
	s_load_dwordx8 s[4:11], s[0:1], 0x0
	s_load_dwordx8 s[12:19], s[0:1], 0x20
	s_load_dwordx2 s[22:23], s[0:1], 0x40
	v_and_b32_e32 v159, 63, v0
	v_lshrrev_b32_e32 v160, 6, v0
	v_and_b32_e32 v143, 3, v159
	v_and_b32_e32 v167, 15, v159
	s_nop 0
	v_readfirstlane_b32 s61, v160
	s_waitcnt lgkmcnt(0)
	s_mov_b64 s[26:27], s[6:7]
	s_mov_b64 s[28:29], s[10:11]
	s_mov_b64 s[24:25], s[14:15]
	s_mov_b64 s[64:65], s[16:17]
	s_mov_b64 s[66:67], s[18:19]
	s_mov_b64 s[68:69], s[8:9]
	s_mov_b32 s8, s4
	s_and_b32 s9, s5, 0xffff
	s_mov_b32 s10, 0x40000000
	s_mov_b32 s11, 0x20000
	s_mov_b32 s12, s68
	s_and_b32 s13, s69, 0xffff
	s_mov_b32 s14, 0x40000000
	s_mov_b32 s15, 0x20000
	s_add_u32 s16, s24, 0x712bd00
	s_addc_u32 s17, s25, 0
	s_add_u32 s18, s16, 0xc35000
	s_addc_u32 s19, s17, 0
	s_add_u32 s20, s16, 0x186a000
	s_addc_u32 s21, s17, 0
	s_sub_u32 s52, s2, 80
	s_mul_i32 s52, s52, 72
	s_add_u32 s32, s52, 72
	s_min_u32 s32, s32, 12500
	s_mov_b32 s40, s64
	s_and_b32 s41, s65, 0xffff
	s_mov_b32 s42, 0x18000
	s_mov_b32 s43, 0x20000
	v_lshlrev_b32_e32 v160, 4, v0
	buffer_load_dwordx4 v[2:5], v160, s[40:43], 0 offen
	v_add_u32_e32 v161, 0x3000, v160
	buffer_load_dwordx4 v[6:9], v161, s[40:43], 0 offen
	v_add_u32_e32 v161, 0x6000, v160
	buffer_load_dwordx4 v[10:13], v161, s[40:43], 0 offen
	v_add_u32_e32 v161, 0x9000, v160
	buffer_load_dwordx4 v[14:17], v161, s[40:43], 0 offen
	v_add_u32_e32 v161, 0xc000, v160
	buffer_load_dwordx4 v[18:21], v161, s[40:43], 0 offen
	v_add_u32_e32 v161, 0xf000, v160
	buffer_load_dwordx4 v[22:25], v161, s[40:43], 0 offen
	v_add_u32_e32 v161, 0x12000, v160
	buffer_load_dwordx4 v[26:29], v161, s[40:43], 0 offen
	v_add_u32_e32 v161, 0x15000, v160
	buffer_load_dwordx4 v[30:33], v161, s[40:43], 0 offen
	v_lshlrev_b32_e32 v162, 2, v0
	v_cmp_gt_u32_e32 vcc, 0x80, v0
	s_and_saveexec_b64 s[58:59], vcc
	s_cbranch_execz .Lfb_nobias
	global_load_dword v163, v162, s[66:67]
.Lfb_nobias:
	s_mov_b64 exec, s[58:59]
	s_waitcnt vmcnt(7)
	ds_write_b128 v160, v[2:5]
	s_waitcnt vmcnt(6)
	v_add_u32_e32 v161, 0x3000, v160
	ds_write_b128 v161, v[6:9]
	s_waitcnt vmcnt(5)
	v_add_u32_e32 v161, 0x6000, v160
	ds_write_b128 v161, v[10:13]
	s_waitcnt vmcnt(4)
	v_add_u32_e32 v161, 0x9000, v160
	ds_write_b128 v161, v[14:17]
	s_waitcnt vmcnt(3)
	v_add_u32_e32 v161, 0xc000, v160
	ds_write_b128 v161, v[18:21]
	s_waitcnt vmcnt(2)
	v_add_u32_e32 v161, 0xf000, v160
	ds_write_b128 v161, v[22:25]
	s_waitcnt vmcnt(1)
	v_add_u32_e32 v161, 0x12000, v160
	ds_write_b128 v161, v[26:29]
	s_waitcnt vmcnt(0)
	v_add_u32_e32 v161, 0x15000, v160
	ds_write_b128 v161, v[30:33]
	s_waitcnt vmcnt(0)
	v_cmp_gt_u32_e32 vcc, 0x80, v0
	s_and_saveexec_b64 s[58:59], vcc
	v_add_u32_e32 v162, 0x24c00, v162
	ds_write_b32 v162, v163
	s_mov_b64 exec, s[58:59]
	v_cmp_eq_u32_e32 vcc, 0, v0
	s_and_saveexec_b64 s[58:59], vcc
	v_mov_b32_e32 v160, 0x24e00
	v_mov_b32_e32 v161, s52
	ds_write_b32 v160, v161
	s_mov_b64 exec, s[58:59]
	s_waitcnt lgkmcnt(0)
	s_barrier
	s_mul_i32 s61, s61, 0x1100
	s_add_u32 s61, s61, 0x18000
	v_lshrrev_b32_e32 v160, 2, v159
	v_lshrrev_b32_e32 v161, 4, v159
	v_lshlrev_b32_e32 v134, 4, v143
	v_mov_b32_e32 v135, v134
	v_mul_u32_u24_e32 v162, 0x110, v160
	v_add3_u32 v136, v162, v134, s61
	v_mul_u32_u24_e32 v162, 0x110, v167
	v_lshl_add_u32 v137, v161, 4, v162
	v_add_u32_e32 v137, s61, v137
	v_lshl_add_u32 v140, v161, 3, v162
	v_add_u32_e32 v140, s61, v140
	v_mul_u32_u24_e32 v162, 0x110, v161
	v_lshl_add_u32 v141, v167, 4, v162
	v_add_u32_e32 v141, s61, v141
	v_lshlrev_b32_e32 v138, 4, v159
	v_add_u32_e32 v139, 0x10000, v138
	v_lshlrev_b32_e32 v142, 8, v161
	v_lshl_add_u32 v142, v167, 4, v142
	v_mov_b32_e32 v144, 0x800000
	v_lshlrev_b32_e32 v145, 2, v160
	v_lshl_add_u32 v145, v143, 6, v145
	v_mul_u32_u24_e32 v146, 0x100, v160
	v_add_u32_e32 v146, v146, v135
	v_mov_b32_e32 v160, 1
	v_mov_b32_e32 v161, 0x24e00
	s_mov_b64 s[58:59], exec
	s_mov_b64 exec, 1
	ds_add_rtn_u32 v160, v161, v160
	s_waitcnt lgkmcnt(0)
	v_readfirstlane_b32 s35, v160
	s_mov_b64 exec, s[58:59]
	s_lshl_b32 s52, s35, 10
	v_add_u32_e32 v160, s52, v145
	global_load_dword v151, v160, s[16:17]
	global_load_dword v152, v160, s[16:17] offset:256
	global_load_dword v153, v160, s[18:19]
	global_load_dword v154, v160, s[18:19] offset:256
	s_lshl_b32 s52, s35, 2
	v_and_b32_e32 v161, 1, v159
	v_mul_u32_u24_e32 v161, 0xc350, v161
	v_add_u32_e32 v161, s52, v161
	global_load_dword v155, v161, s[20:21]
	s_waitcnt vmcnt(0)
	s_mov_b32 s34, s35
	v_readlane_b32 s52, v155, 0
	v_readlane_b32 s53, v155, 1
	s_cmp_lt_u32 s34, s32
	s_cselect_b32 s47, s52, 0
	s_cselect_b32 s48, s53, 0
	s_max_u32 s38, s47, 2
	s_max_u32 s39, s48, 2
	v_cmp_gt_i32_e32 vcc, s47, v143
	s_nop 1
	v_cndmask_b32_e32 v147, v144, v151, vcc
	v_mov_b32_e32 v148, v152
	v_mov_b32_e32 v149, v153
	v_mov_b32_e32 v150, v154
	s_mov_b32 s44, 0
	s_mov_b32 s46, 0
	s_mov_b32 s45, s38
	s_mov_b64 s[40:41], s[8:9]
	s_mov_b64 s[42:43], s[10:11]
	s_movk_i32 s49, 0x100
	s_mov_b32 s70, 0
	v_mov_b32_e32 v160, 1
	v_mov_b32_e32 v161, 0x24e00
	s_mov_b64 s[58:59], exec
	s_mov_b64 exec, 1
	ds_add_rtn_u32 v160, v161, v160
	s_waitcnt lgkmcnt(0)
	v_readfirstlane_b32 s35, v160
	s_mov_b64 exec, s[58:59]
	s_lshl_b32 s52, s35, 10
	v_add_u32_e32 v160, s52, v145
	global_load_dword v151, v160, s[16:17]
	global_load_dword v152, v160, s[16:17] offset:256
	global_load_dword v153, v160, s[18:19]
	global_load_dword v154, v160, s[18:19] offset:256
	s_lshl_b32 s52, s35, 2
	v_and_b32_e32 v161, 1, v159
	v_mul_u32_u24_e32 v161, 0xc350, v161
	v_add_u32_e32 v161, s52, v161
	global_load_dword v155, v161, s[20:21]
	s_mov_b32 s64, 2
	s_mov_b32 s66, 0

.Lfb_pe1:
	ds_read_b128 v[126:129], v137
	ds_read_b128 v[114:117], v138 offset:32768
	ds_read_b128 v[118:121], v138 offset:33792
	ds_read_b128 v[122:125], v138 offset:34816
	s_waitcnt lgkmcnt(2)
	v_mfma_f32_16x16x32_f16 v[82:85], v[114:117], v[126:129], v[82:85]
	ds_read_b128 v[114:117], v138 offset:35840
	s_waitcnt lgkmcnt(2)
	v_mfma_f32_16x16x32_f16 v[86:89], v[118:121], v[126:129], v[86:89]
	ds_read_b128 v[118:121], v138 offset:36864
	s_waitcnt lgkmcnt(2)
	v_mfma_f32_16x16x32_f16 v[90:93], v[122:125], v[126:129], v[90:93]
	ds_read_b128 v[122:125], v138 offset:37888
	s_waitcnt lgkmcnt(2)
	v_mfma_f32_16x16x32_f16 v[94:97], v[114:117], v[126:129], v[94:97]
	ds_read_b128 v[114:117], v138 offset:38912
	s_waitcnt lgkmcnt(2)
	v_mfma_f32_16x16x32_f16 v[98:101], v[118:121], v[126:129], v[98:101]
	ds_read_b128 v[118:121], v138 offset:39936
	s_waitcnt lgkmcnt(2)
	v_mfma_f32_16x16x32_f16 v[102:105], v[122:125], v[126:129], v[102:105]
	ds_read_b128 v[130:133], v137 offset:64
	ds_read_b128 v[122:125], v138 offset:40960
	s_waitcnt lgkmcnt(3)
	v_mfma_f32_16x16x32_f16 v[106:109], v[114:117], v[126:129], v[106:109]
	ds_read_b128 v[114:117], v138 offset:41984
	s_waitcnt lgkmcnt(3)
	v_mfma_f32_16x16x32_f16 v[110:113], v[118:121], v[126:129], v[110:113]
	ds_read_b128 v[118:121], v138 offset:43008
	s_waitcnt lgkmcnt(2)
	v_mfma_f32_16x16x32_f16 v[82:85], v[122:125], v[130:133], v[82:85]
	ds_read_b128 v[122:125], v138 offset:44032
	s_waitcnt lgkmcnt(2)
	v_mfma_f32_16x16x32_f16 v[86:89], v[114:117], v[130:133], v[86:89]
	ds_read_b128 v[114:117], v138 offset:45056
	s_waitcnt lgkmcnt(2)
	v_mfma_f32_16x16x32_f16 v[90:93], v[118:121], v[130:133], v[90:93]
	ds_read_b128 v[118:121], v138 offset:46080
	s_waitcnt lgkmcnt(2)
	v_mfma_f32_16x16x32_f16 v[94:97], v[122:125], v[130:133], v[94:97]
	ds_read_b128 v[122:125], v138 offset:47104
	s_waitcnt lgkmcnt(2)
	v_mfma_f32_16x16x32_f16 v[98:101], v[114:117], v[130:133], v[98:101]
	ds_read_b128 v[114:117], v138 offset:48128
	s_waitcnt lgkmcnt(2)
	v_mfma_f32_16x16x32_f16 v[102:105], v[118:121], v[130:133], v[102:105]
	ds_read_b128 v[126:129], v137 offset:128
	ds_read_b128 v[118:121], v138 offset:49152
	s_waitcnt lgkmcnt(3)
	v_mfma_f32_16x16x32_f16 v[106:109], v[122:125], v[130:133], v[106:109]
	ds_read_b128 v[122:125], v138 offset:50176
	s_waitcnt lgkmcnt(3)
	v_mfma_f32_16x16x32_f16 v[110:113], v[114:117], v[130:133], v[110:113]
	ds_read_b128 v[114:117], v138 offset:51200
	s_waitcnt lgkmcnt(2)
	v_mfma_f32_16x16x32_f16 v[82:85], v[118:121], v[126:129], v[82:85]
	ds_read_b128 v[118:121], v138 offset:52224
	s_waitcnt lgkmcnt(2)
	v_mfma_f32_16x16x32_f16 v[86:89], v[122:125], v[126:129], v[86:89]
	ds_read_b128 v[122:125], v138 offset:53248
	s_waitcnt lgkmcnt(2)
	v_mfma_f32_16x16x32_f16 v[90:93], v[114:117], v[126:129], v[90:93]
	ds_read_b128 v[114:117], v138 offset:54272
	s_waitcnt lgkmcnt(2)
	v_mfma_f32_16x16x32_f16 v[94:97], v[118:121], v[126:129], v[94:97]
	ds_read_b128 v[118:121], v138 offset:55296
	s_waitcnt lgkmcnt(2)
	v_mfma_f32_16x16x32_f16 v[98:101], v[122:125], v[126:129], v[98:101]
	ds_read_b128 v[122:125], v138 offset:56320
	s_waitcnt lgkmcnt(2)
	v_mfma_f32_16x16x32_f16 v[102:105], v[114:117], v[126:129], v[102:105]
	ds_read_b128 v[130:133], v137 offset:192
	ds_read_b128 v[114:117], v138 offset:57344
	s_waitcnt lgkmcnt(3)
	v_mfma_f32_16x16x32_f16 v[106:109], v[118:121], v[126:129], v[106:109]
	ds_read_b128 v[118:121], v138 offset:58368
	s_waitcnt lgkmcnt(3)
	v_mfma_f32_16x16x32_f16 v[110:113], v[122:125], v[126:129], v[110:113]
	ds_read_b128 v[122:125], v138 offset:59392
	s_waitcnt lgkmcnt(2)
	v_mfma_f32_16x16x32_f16 v[82:85], v[114:117], v[130:133], v[82:85]
	ds_read_b128 v[114:117], v138 offset:60416
	s_waitcnt lgkmcnt(2)
	v_mfma_f32_16x16x32_f16 v[86:89], v[118:121], v[130:133], v[86:89]
	ds_read_b128 v[118:121], v138 offset:61440
	s_waitcnt lgkmcnt(2)
	v_mfma_f32_16x16x32_f16 v[90:93], v[122:125], v[130:133], v[90:93]
	ds_read_b128 v[122:125], v138 offset:62464
	s_waitcnt lgkmcnt(2)
	v_mfma_f32_16x16x32_f16 v[94:97], v[114:117], v[130:133], v[94:97]
	ds_read_b128 v[114:117], v138 offset:63488
	s_waitcnt lgkmcnt(2)
	v_mfma_f32_16x16x32_f16 v[98:101], v[118:121], v[130:133], v[98:101]
	ds_read_b128 v[118:121], v138 offset:64512
	s_waitcnt lgkmcnt(2)
	v_mfma_f32_16x16x32_f16 v[102:105], v[122:125], v[130:133], v[102:105]
	s_waitcnt lgkmcnt(1)
	v_mfma_f32_16x16x32_f16 v[106:109], v[114:117], v[130:133], v[106:109]
	s_waitcnt lgkmcnt(0)
	v_mfma_f32_16x16x32_f16 v[110:113], v[118:121], v[130:133], v[110:113]
	s_mov_b32 s64, 1
	s_cmp_eq_u32 s51, 0
	s_cbranch_scc1 .Lfb_is_0
	s_cmp_eq_u32 s51, 1
	s_cbranch_scc1 .Lfb_is_1
	s_cmp_eq_u32 s51, 2
	s_cbranch_scc1 .Lfb_is_2
	s_branch .Lfb_is_3
.Lfb_tileend:
	ds_read_b128 v[126:129], v137
	ds_read_b128 v[114:117], v139
	ds_read_b128 v[118:121], v139 offset:1024
	ds_read_b128 v[122:125], v139 offset:2048
	s_waitcnt lgkmcnt(2)
	v_mfma_f32_16x16x32_f16 v[82:85], v[114:117], v[126:129], v[82:85]
	ds_read_b128 v[114:117], v139 offset:3072
	s_waitcnt lgkmcnt(2)
	v_mfma_f32_16x16x32_f16 v[86:89], v[118:121], v[126:129], v[86:89]
	ds_read_b128 v[118:121], v139 offset:4096
	s_waitcnt lgkmcnt(2)
	v_mfma_f32_16x16x32_f16 v[90:93], v[122:125], v[126:129], v[90:93]
	ds_read_b128 v[122:125], v139 offset:5120
	s_waitcnt lgkmcnt(2)
	v_mfma_f32_16x16x32_f16 v[94:97], v[114:117], v[126:129], v[94:97]
	ds_read_b128 v[114:117], v139 offset:6144
	s_waitcnt lgkmcnt(2)
	v_mfma_f32_16x16x32_f16 v[98:101], v[118:121], v[126:129], v[98:101]
	ds_read_b128 v[118:121], v139 offset:7168
	s_waitcnt lgkmcnt(2)
	v_mfma_f32_16x16x32_f16 v[102:105], v[122:125], v[126:129], v[102:105]
	ds_read_b128 v[130:133], v137 offset:64
	ds_read_b128 v[122:125], v139 offset:8192
	s_waitcnt lgkmcnt(3)
	v_mfma_f32_16x16x32_f16 v[106:109], v[114:117], v[126:129], v[106:109]
	ds_read_b128 v[114:117], v139 offset:9216
	s_waitcnt lgkmcnt(3)
	v_mfma_f32_16x16x32_f16 v[110:113], v[118:121], v[126:129], v[110:113]
	ds_read_b128 v[118:121], v139 offset:10240
	s_waitcnt lgkmcnt(2)
	v_mfma_f32_16x16x32_f16 v[82:85], v[122:125], v[130:133], v[82:85]
	ds_read_b128 v[122:125], v139 offset:11264
	s_waitcnt lgkmcnt(2)
	v_mfma_f32_16x16x32_f16 v[86:89], v[114:117], v[130:133], v[86:89]
	ds_read_b128 v[114:117], v139 offset:12288
	s_waitcnt lgkmcnt(2)
	v_mfma_f32_16x16x32_f16 v[90:93], v[118:121], v[130:133], v[90:93]
	ds_read_b128 v[118:121], v139 offset:13312
	s_waitcnt lgkmcnt(2)
	v_mfma_f32_16x16x32_f16 v[94:97], v[122:125], v[130:133], v[94:97]
	ds_read_b128 v[122:125], v139 offset:14336
	s_waitcnt lgkmcnt(2)
	v_mfma_f32_16x16x32_f16 v[98:101], v[114:117], v[130:133], v[98:101]
	ds_read_b128 v[114:117], v139 offset:15360
	s_waitcnt lgkmcnt(2)
	v_mfma_f32_16x16x32_f16 v[102:105], v[118:121], v[130:133], v[102:105]
	ds_read_b128 v[126:129], v137 offset:128
	ds_read_b128 v[118:121], v139 offset:16384
	s_waitcnt lgkmcnt(3)
	v_mfma_f32_16x16x32_f16 v[106:109], v[122:125], v[130:133], v[106:109]
	ds_read_b128 v[122:125], v139 offset:17408
	s_waitcnt lgkmcnt(3)
	v_mfma_f32_16x16x32_f16 v[110:113], v[114:117], v[130:133], v[110:113]
	ds_read_b128 v[114:117], v139 offset:18432
	s_waitcnt lgkmcnt(2)
	v_mfma_f32_16x16x32_f16 v[82:85], v[118:121], v[126:129], v[82:85]
	ds_read_b128 v[118:121], v139 offset:19456
	s_waitcnt lgkmcnt(2)
	v_mfma_f32_16x16x32_f16 v[86:89], v[122:125], v[126:129], v[86:89]
	ds_read_b128 v[122:125], v139 offset:20480
	s_waitcnt lgkmcnt(2)
	v_mfma_f32_16x16x32_f16 v[90:93], v[114:117], v[126:129], v[90:93]
	ds_read_b128 v[114:117], v139 offset:21504
	s_waitcnt lgkmcnt(2)
	v_mfma_f32_16x16x32_f16 v[94:97], v[118:121], v[126:129], v[94:97]
	ds_read_b128 v[118:121], v139 offset:22528
	s_waitcnt lgkmcnt(2)
	v_mfma_f32_16x16x32_f16 v[98:101], v[122:125], v[126:129], v[98:101]
	ds_read_b128 v[122:125], v139 offset:23552
	s_waitcnt lgkmcnt(2)
	v_mfma_f32_16x16x32_f16 v[102:105], v[114:117], v[126:129], v[102:105]
	ds_read_b128 v[130:133], v137 offset:192
	ds_read_b128 v[114:117], v139 offset:24576
	s_waitcnt lgkmcnt(3)
	v_mfma_f32_16x16x32_f16 v[106:109], v[118:121], v[126:129], v[106:109]
	ds_read_b128 v[118:121], v139 offset:25600
	s_waitcnt lgkmcnt(3)
	v_mfma_f32_16x16x32_f16 v[110:113], v[122:125], v[126:129], v[110:113]
	ds_read_b128 v[122:125], v139 offset:26624
	s_waitcnt lgkmcnt(2)
	v_mfma_f32_16x16x32_f16 v[82:85], v[114:117], v[130:133], v[82:85]
	ds_read_b128 v[114:117], v139 offset:27648
	s_waitcnt lgkmcnt(2)
	v_mfma_f32_16x16x32_f16 v[86:89], v[118:121], v[130:133], v[86:89]
	ds_read_b128 v[118:121], v139 offset:28672
	s_waitcnt lgkmcnt(2)
	v_mfma_f32_16x16x32_f16 v[90:93], v[122:125], v[130:133], v[90:93]
	ds_read_b128 v[122:125], v139 offset:29696
	s_waitcnt lgkmcnt(2)
	v_mfma_f32_16x16x32_f16 v[94:97], v[114:117], v[130:133], v[94:97]
	ds_read_b128 v[114:117], v139 offset:30720
	s_waitcnt lgkmcnt(2)
	v_mfma_f32_16x16x32_f16 v[98:101], v[118:121], v[130:133], v[98:101]
	ds_read_b128 v[118:121], v139 offset:31744
	s_waitcnt lgkmcnt(2)
	v_mfma_f32_16x16x32_f16 v[102:105], v[122:125], v[130:133], v[102:105]
	s_waitcnt lgkmcnt(1)
	v_mfma_f32_16x16x32_f16 v[106:109], v[114:117], v[130:133], v[106:109]
	s_waitcnt lgkmcnt(0)
	v_mfma_f32_16x16x32_f16 v[110:113], v[118:121], v[130:133], v[110:113]
	s_nop 7
	s_nop 3
	v_max_f32_e32 v82, 0, v82
	v_max_f32_e32 v83, 0, v83
	v_max_f32_e32 v84, 0, v84
	v_max_f32_e32 v85, 0, v85
	v_cvt_pk_f16_f32 v160, v82, v83
	v_cvt_pk_f16_f32 v161, v84, v85
	ds_write_b64 v140, v[160:161]
	v_max_f32_e32 v86, 0, v86
	v_max_f32_e32 v87, 0, v87
	v_max_f32_e32 v88, 0, v88
	v_max_f32_e32 v89, 0, v89
	v_cvt_pk_f16_f32 v162, v86, v87
	v_cvt_pk_f16_f32 v163, v88, v89
	ds_write_b64 v140, v[162:163] offset:32
	v_max_f32_e32 v90, 0, v90
	v_max_f32_e32 v91, 0, v91
	v_max_f32_e32 v92, 0, v92
	v_max_f32_e32 v93, 0, v93
	v_cvt_pk_f16_f32 v160, v90, v91
	v_cvt_pk_f16_f32 v161, v92, v93
	ds_write_b64 v140, v[160:161] offset:64
	v_max_f32_e32 v94, 0, v94
	v_max_f32_e32 v95, 0, v95
	v_max_f32_e32 v96, 0, v96
	v_max_f32_e32 v97, 0, v97
	v_cvt_pk_f16_f32 v162, v94, v95
	v_cvt_pk_f16_f32 v163, v96, v97
	ds_write_b64 v140, v[162:163] offset:96
	v_max_f32_e32 v98, 0, v98
	v_max_f32_e32 v99, 0, v99
	v_max_f32_e32 v100, 0, v100
	v_max_f32_e32 v101, 0, v101
	v_cvt_pk_f16_f32 v160, v98, v99
	v_cvt_pk_f16_f32 v161, v100, v101
	ds_write_b64 v140, v[160:161] offset:128
	v_max_f32_e32 v102, 0, v102
	v_max_f32_e32 v103, 0, v103
	v_max_f32_e32 v104, 0, v104
	v_max_f32_e32 v105, 0, v105
	v_cvt_pk_f16_f32 v162, v102, v103
	v_cvt_pk_f16_f32 v163, v104, v105
	ds_write_b64 v140, v[162:163] offset:160
	v_max_f32_e32 v106, 0, v106
	v_max_f32_e32 v107, 0, v107
	v_max_f32_e32 v108, 0, v108
	v_max_f32_e32 v109, 0, v109
	v_cvt_pk_f16_f32 v160, v106, v107
	v_cvt_pk_f16_f32 v161, v108, v109
	ds_write_b64 v140, v[160:161] offset:192
	v_max_f32_e32 v110, 0, v110
	v_max_f32_e32 v111, 0, v111
	v_max_f32_e32 v112, 0, v112
	v_max_f32_e32 v113, 0, v113
	v_cvt_pk_f16_f32 v162, v110, v111
	v_cvt_pk_f16_f32 v163, v112, v113
	ds_write_b64 v140, v[162:163] offset:224
	s_lshl_b32 s52, s33, 12
	v_add_u32_e32 v158, s52, v142
	ds_read_b128 v[114:117], v141
	ds_read_b128 v[118:121], v141 offset:1088
	ds_read_b128 v[122:125], v141 offset:2176
	ds_read_b128 v[126:129], v141 offset:3264
	s_waitcnt lgkmcnt(3)
	global_store_dwordx4 v158, v[114:117], s[22:23] sc1
	s_waitcnt lgkmcnt(2)
	global_store_dwordx4 v158, v[118:121], s[22:23] offset:1024 sc1
	s_waitcnt lgkmcnt(1)
	global_store_dwordx4 v158, v[122:125], s[22:23] offset:2048 sc1
	s_waitcnt lgkmcnt(0)
	global_store_dwordx4 v158, v[126:129], s[22:23] offset:3072 sc1
	s_nop 1
	s_mov_b32 s66, 0
	s_branch .Lfb_tilestart
.Lfb_exit:
	s_endpgm
.LBB6_69:
	s_and_b64 vcc, exec, s[4:5]
	s_cbranch_vccz .LBB6_123
	s_load_dwordx2 s[4:5], s[0:1], 0x98
	s_load_dword s10, s[0:1], 0xb4
	v_mov_b32_e32 v131, 0
	s_movk_i32 s6, 0x3000
	s_waitcnt vmcnt(13)
	v_or_b32_e32 v24, 0xc000, v130
	s_waitcnt lgkmcnt(0)
	v_lshl_add_u64 v[26:27], s[4:5], 0, v[130:131]
	s_waitcnt vmcnt(1)
	v_add_co_u32_e32 v10, vcc, s6, v26
	s_movk_i32 s6, 0x6000
	s_nop 0
	v_addc_co_u32_e32 v11, vcc, 0, v27, vcc
	v_add_co_u32_e32 v12, vcc, s6, v26
	s_mov_b32 s6, 0x9000
	s_nop 0
	v_addc_co_u32_e32 v13, vcc, 0, v27, vcc
	v_add_co_u32_e32 v22, vcc, s6, v26
	global_load_dwordx4 v[2:5], v130, s[4:5]
	s_nop 0
	v_addc_co_u32_e32 v23, vcc, 0, v27, vcc
	global_load_dwordx4 v[14:17], v[10:11], off
	global_load_dwordx4 v[6:9], v[12:13], off
	global_load_dwordx4 v[18:21], v[22:23], off
	s_nop 0
	global_load_dwordx4 v[10:13], v24, s[4:5]
	s_abs_i32 s8, s3
	v_cvt_f32_u32_e32 v22, s8
	s_sub_i32 s4, 0, s8
	s_add_i32 s11, s3, s10
	s_add_i32 s11, s11, -1
	v_rcp_iflag_f32_e32 v22, v22
	s_abs_i32 s9, s11
	v_mov_b32_e32 v23, v131
	v_mov_b32_e32 v24, v131
	v_mul_f32_e32 v22, 0x4f7ffffe, v22
	v_cvt_u32_f32_e32 v22, v22
	v_mov_b32_e32 v25, v131
	v_readfirstlane_b32 s12, v22
	s_mul_i32 s4, s4, s12
	s_mul_hi_u32 s4, s12, s4
	s_add_i32 s12, s12, s4
	s_movk_i32 s4, 0x100
	v_cmp_gt_u32_e64 s[4:5], s4, v0
	s_and_saveexec_b64 s[6:7], s[4:5]
	s_cbranch_execz .LBB6_72
	v_add_co_u32_e32 v22, vcc, 0xf000, v26
	s_nop 1
	v_addc_co_u32_e32 v23, vcc, 0, v27, vcc
	global_load_dwordx4 v[22:25], v[22:23], off
	s_waitcnt vmcnt(0)
	v_mov_b32_e32 v131, v22

	.amdhsa_kernel _Z10k_layer_fhILi128ELb1EEv9LayerArgsS0_i
		.amdhsa_group_segment_fixed_size 151044
		.amdhsa_private_segment_fixed_size 0
		.amdhsa_kernarg_size 472
		.amdhsa_user_sgpr_count 2
		.amdhsa_user_sgpr_dispatch_ptr 0
		.amdhsa_user_sgpr_queue_ptr 0
		.amdhsa_user_sgpr_kernarg_segment_ptr 1
		.amdhsa_user_sgpr_dispatch_id 0
		.amdhsa_user_sgpr_kernarg_preload_length 0
		.amdhsa_user_sgpr_kernarg_preload_offset 0
		.amdhsa_user_sgpr_private_segment_size 0
		.amdhsa_uses_dynamic_stack 0
		.amdhsa_enable_private_segment 0
		.amdhsa_system_sgpr_workgroup_id_x 1
		.amdhsa_system_sgpr_workgroup_id_y 0
		.amdhsa_system_sgpr_workgroup_id_z 0
		.amdhsa_system_sgpr_workgroup_info 0
		.amdhsa_system_vgpr_workitem_id 0
		.amdhsa_next_free_vgpr 168
		.amdhsa_next_free_sgpr 96
		.amdhsa_accum_offset 168
		.amdhsa_reserve_vcc 1
		.amdhsa_float_round_mode_32 0
		.amdhsa_float_round_mode_16_64 0
		.amdhsa_float_denorm_mode_32 3
		.amdhsa_float_denorm_mode_16_64 3
		.amdhsa_dx10_clamp 1
		.amdhsa_ieee_mode 1
		.amdhsa_fp16_overflow 0
		.amdhsa_tg_split 0
		.amdhsa_exception_fp_ieee_invalid_op 0
		.amdhsa_exception_fp_denorm_src 0
		.amdhsa_exception_fp_ieee_div_zero 0
		.amdhsa_exception_fp_ieee_overflow 0
		.amdhsa_exception_fp_ieee_underflow 0
		.amdhsa_exception_fp_ieee_inexact 0
		.amdhsa_exception_int_div_zero 0
	.end_amdhsa_kernel
	.text
.Lfunc_end6:
	.size	_Z10k_layer_fhILi128ELb1EEv9LayerArgsS0_i, .Lfunc_end6-_Z10k_layer_fhILi128ELb1EEv9LayerArgsS0_i
	.set _Z10k_layer_fhILi128ELb1EEv9LayerArgsS0_i.num_vgpr, 166
	.set _Z10k_layer_fhILi128ELb1EEv9LayerArgsS0_i.num_agpr, 0
	.set _Z10k_layer_fhILi128ELb1EEv9LayerArgsS0_i.numbered_sgpr, 39
	.set _Z10k_layer_fhILi128ELb1EEv9LayerArgsS0_i.num_named_barrier, 0
	.set _Z10k_layer_fhILi128ELb1EEv9LayerArgsS0_i.private_seg_size, 0
	.set _Z10k_layer_fhILi128ELb1EEv9LayerArgsS0_i.uses_vcc, 1
	.set _Z10k_layer_fhILi128ELb1EEv9LayerArgsS0_i.uses_flat_scratch, 0
	.set _Z10k_layer_fhILi128ELb1EEv9LayerArgsS0_i.has_dyn_sized_stack, 0
	.set _Z10k_layer_fhILi128ELb1EEv9LayerArgsS0_i.has_recursion, 0
	.set _Z10k_layer_fhILi128ELb1EEv9LayerArgsS0_i.has_indirect_call, 0

amdhsa.kernels:
  - .agpr_count:     0
    .args:
      - .actual_access:  read_only
        .address_space:  global
        .offset:         0
        .size:           8
        .value_kind:     global_buffer
      - .actual_access:  read_only
        .address_space:  global
        .offset:         8
        .size:           8
        .value_kind:     global_buffer
      - .actual_access:  write_only
        .address_space:  global
        .offset:         16
        .size:           8
        .value_kind:     global_buffer
      - .address_space:  global
        .offset:         24
        .size:           8
        .value_kind:     global_buffer
    .group_segment_fixed_size: 16400
    .kernarg_segment_align: 8
    .kernarg_segment_size: 32
    .language:       OpenCL C
    .language_version:
      - 2
      - 0
    .max_flat_workgroup_size: 256
    .name:           _Z6k_bcsrPK15HIP_vector_typeIiLj2EEPKiPiS5_
    .private_segment_fixed_size: 0
    .sgpr_count:     28
    .sgpr_spill_count: 0
    .symbol:         _Z6k_bcsrPK15HIP_vector_typeIiLj2EEPKiPiS5_.kd
    .uniform_work_group_size: 1
    .uses_dynamic_stack: false
    .vgpr_count:     28
    .vgpr_spill_count: 0
    .wavefront_size: 64
  - .agpr_count:     0
    .args:
      - .actual_access:  read_only
        .address_space:  global
        .offset:         0
        .size:           8
        .value_kind:     global_buffer
      - .actual_access:  read_only
        .address_space:  global
        .offset:         8
        .size:           8
        .value_kind:     global_buffer
      - .actual_access:  read_only
        .address_space:  global
        .offset:         16
        .size:           8
        .value_kind:     global_buffer
      - .actual_access:  write_only
        .address_space:  global
        .offset:         24
        .size:           8
        .value_kind:     global_buffer
      - .actual_access:  write_only
        .address_space:  global
        .offset:         32
        .size:           8
        .value_kind:     global_buffer
      - .actual_access:  read_only
        .address_space:  global
        .offset:         40
        .size:           8
        .value_kind:     global_buffer
      - .actual_access:  read_only
        .address_space:  global
        .offset:         48
        .size:           8
        .value_kind:     global_buffer
      - .actual_access:  read_only
        .address_space:  global
        .offset:         56
        .size:           8
        .value_kind:     global_buffer
      - .actual_access:  read_only
        .address_space:  global
        .offset:         64
        .size:           8
        .value_kind:     global_buffer
      - .actual_access:  read_only
        .address_space:  global
        .offset:         72
        .size:           8
        .value_kind:     global_buffer
      - .actual_access:  read_only
        .address_space:  global
        .offset:         80
        .size:           8
        .value_kind:     global_buffer
      - .actual_access:  read_only
        .address_space:  global
        .offset:         88
        .size:           8
        .value_kind:     global_buffer
      - .actual_access:  read_only
        .address_space:  global
        .offset:         96
        .size:           8
        .value_kind:     global_buffer
      - .address_space:  global
        .offset:         104
        .size:           8
        .value_kind:     global_buffer
      - .address_space:  global
        .offset:         112
        .size:           8
        .value_kind:     global_buffer
    .group_segment_fixed_size: 4384
    .kernarg_segment_align: 8
    .kernarg_segment_size: 120
    .language:       OpenCL C
    .language_version:
      - 2
      - 0
    .max_flat_workgroup_size: 1024
    .name:           _Z8k_bcountPKiS0_S0_PiPjPKfS4_S0_S0_S0_S4_S4_S4_PDF16_S5_
    .private_segment_fixed_size: 0
    .sgpr_count:     26
    .sgpr_spill_count: 0
    .symbol:         _Z8k_bcountPKiS0_S0_PiPjPKfS4_S0_S0_S0_S4_S4_S4_PDF16_S5_.kd
    .uniform_work_group_size: 1
    .uses_dynamic_stack: false
    .vgpr_count:     21
    .vgpr_spill_count: 0
    .wavefront_size: 64
  - .agpr_count:     0
    .args:
      - .actual_access:  read_only
        .address_space:  global
        .offset:         0
        .size:           8
        .value_kind:     global_buffer
      - .actual_access:  read_only
        .address_space:  global
        .offset:         8
        .size:           8
        .value_kind:     global_buffer
      - .actual_access:  read_only
        .address_space:  global
        .offset:         16
        .size:           8
        .value_kind:     global_buffer
      - .actual_access:  read_only
        .address_space:  global
        .offset:         24
        .size:           8
        .value_kind:     global_buffer
      - .actual_access:  write_only
        .address_space:  global
        .offset:         32
        .size:           8
        .value_kind:     global_buffer
      - .actual_access:  write_only
        .address_space:  global
        .offset:         40
        .size:           8
        .value_kind:     global_buffer
      - .actual_access:  read_only
        .address_space:  global
        .offset:         48
        .size:           8
        .value_kind:     global_buffer
      - .actual_access:  read_only
        .address_space:  global
        .offset:         56
        .size:           8
        .value_kind:     global_buffer
      - .actual_access:  read_only
        .address_space:  global
        .offset:         64
        .size:           8
        .value_kind:     global_buffer
      - .actual_access:  read_only
        .address_space:  global
        .offset:         72
        .size:           8
        .value_kind:     global_buffer
      - .actual_access:  read_only
        .address_space:  global
        .offset:         80
        .size:           8
        .value_kind:     global_buffer
      - .actual_access:  read_only
        .address_space:  global
        .offset:         88
        .size:           8
        .value_kind:     global_buffer
      - .actual_access:  read_only
        .address_space:  global
        .offset:         96
        .size:           8
        .value_kind:     global_buffer
      - .actual_access:  read_only
        .address_space:  global
        .offset:         104
        .size:           8
        .value_kind:     global_buffer
      - .address_space:  global
        .offset:         112
        .size:           8
        .value_kind:     global_buffer
      - .address_space:  global
        .offset:         120
        .size:           8
        .value_kind:     global_buffer
      - .offset:         128
        .size:           488
        .value_kind:     by_value
    .group_segment_fixed_size: 17024
    .kernarg_segment_align: 8
    .kernarg_segment_size: 616
    .language:       OpenCL C
    .language_version:
      - 2
      - 0
    .max_flat_workgroup_size: 1024
    .name:           _Z6k_prepPKiS0_S0_S0_PiP15HIP_vector_typeIiLj2EEPKfS6_S0_S0_S0_S6_S6_S6_PDF16_S7_6WSpecs
    .private_segment_fixed_size: 0
    .sgpr_count:     44
    .sgpr_spill_count: 0
    .symbol:         _Z6k_prepPKiS0_S0_S0_PiP15HIP_vector_typeIiLj2EEPKfS6_S0_S0_S0_S6_S6_S6_PDF16_S7_6WSpecs.kd
    .uniform_work_group_size: 1
    .uses_dynamic_stack: false
    .vgpr_count:     82
    .vgpr_spill_count: 0
    .wavefront_size: 64
  - .agpr_count:     0
    .args:
      - .offset:         0
        .size:           104
        .value_kind:     by_value
      - .offset:         104
        .size:           4
        .value_kind:     hidden_block_count_x
      - .offset:         108
        .size:           4
        .value_kind:     hidden_block_count_y
      - .offset:         112
        .size:           4
        .value_kind:     hidden_block_count_z
      - .offset:         116
        .size:           2
        .value_kind:     hidden_group_size_x
      - .offset:         118
        .size:           2
        .value_kind:     hidden_group_size_y
      - .offset:         120
        .size:           2
        .value_kind:     hidden_group_size_z
      - .offset:         122
        .size:           2
        .value_kind:     hidden_remainder_x
      - .offset:         124
        .size:           2
        .value_kind:     hidden_remainder_y
      - .offset:         126
        .size:           2
        .value_kind:     hidden_remainder_z
      - .offset:         144
        .size:           8
        .value_kind:     hidden_global_offset_x
      - .offset:         152
        .size:           8
        .value_kind:     hidden_global_offset_y
      - .offset:         160
        .size:           8
        .value_kind:     hidden_global_offset_z
      - .offset:         168
        .size:           2
        .value_kind:     hidden_grid_dims
    .group_segment_fixed_size: 155140
    .kernarg_segment_align: 8
    .kernarg_segment_size: 360
    .language:       OpenCL C
    .language_version:
      - 2
      - 0
    .max_flat_workgroup_size: 768
    .name:           _Z12k_layer_pool9LayerArgs
    .private_segment_fixed_size: 0
    .sgpr_count:     50
    .sgpr_spill_count: 0
    .symbol:         _Z12k_layer_pool9LayerArgs.kd
    .uniform_work_group_size: 1
    .uses_dynamic_stack: false
    .vgpr_count:     168
    .vgpr_spill_count: 0
    .wavefront_size: 64
  - .agpr_count:     0
    .args:
      - .actual_access:  read_only
        .address_space:  global
        .offset:         0
        .size:           8
        .value_kind:     global_buffer
      - .actual_access:  read_only
        .address_space:  global
        .offset:         8
        .size:           8
        .value_kind:     global_buffer
      - .actual_access:  read_only
        .address_space:  global
        .offset:         16
        .size:           8
        .value_kind:     global_buffer
      - .actual_access:  read_only
        .address_space:  global
        .offset:         24
        .size:           8
        .value_kind:     global_buffer
      - .actual_access:  read_only
        .address_space:  global
        .offset:         32
        .size:           8
        .value_kind:     global_buffer
      - .actual_access:  read_only
        .address_space:  global
        .offset:         40
        .size:           8
        .value_kind:     global_buffer
      - .actual_access:  read_only
        .address_space:  global
        .offset:         48
        .size:           8
        .value_kind:     global_buffer
      - .actual_access:  write_only
        .address_space:  global
        .offset:         56
        .size:           8
        .value_kind:     global_buffer
    .group_segment_fixed_size: 2560
    .kernarg_segment_align: 8
    .kernarg_segment_size: 64
    .language:       OpenCL C
    .language_version:
      - 2
      - 0
    .max_flat_workgroup_size: 512
    .name:           _Z5k_mlpPKjPKfS2_S2_S2_S2_S2_Pf
    .private_segment_fixed_size: 0
    .sgpr_count:     18
    .sgpr_spill_count: 0
    .symbol:         _Z5k_mlpPKjPKfS2_S2_S2_S2_S2_Pf.kd
    .uniform_work_group_size: 1
    .uses_dynamic_stack: false
    .vgpr_count:     120
    .vgpr_spill_count: 0
    .wavefront_size: 64
  - .agpr_count:     0
    .args:
      - .offset:         0
        .size:           104
        .value_kind:     by_value
      - .offset:         104
        .size:           104
        .value_kind:     by_value
      - .offset:         208
        .size:           4
        .value_kind:     by_value
      - .offset:         216
        .size:           4
        .value_kind:     hidden_block_count_x
      - .offset:         220
        .size:           4
        .value_kind:     hidden_block_count_y
      - .offset:         224
        .size:           4
        .value_kind:     hidden_block_count_z
      - .offset:         228
        .size:           2
        .value_kind:     hidden_group_size_x
      - .offset:         230
        .size:           2
        .value_kind:     hidden_group_size_y
      - .offset:         232
        .size:           2
        .value_kind:     hidden_group_size_z
      - .offset:         234
        .size:           2
        .value_kind:     hidden_remainder_x
      - .offset:         236
        .size:           2
        .value_kind:     hidden_remainder_y
      - .offset:         238
        .size:           2
        .value_kind:     hidden_remainder_z
      - .offset:         256
        .size:           8
        .value_kind:     hidden_global_offset_x
      - .offset:         264
        .size:           8
        .value_kind:     hidden_global_offset_y
      - .offset:         272
        .size:           8
        .value_kind:     hidden_global_offset_z
      - .offset:         280
        .size:           2
        .value_kind:     hidden_grid_dims
    .group_segment_fixed_size: 151044
    .kernarg_segment_align: 8
    .kernarg_segment_size: 472
    .language:       OpenCL C
    .language_version:
      - 2
      - 0
    .max_flat_workgroup_size: 768
    .name:           _Z10k_layer_fhILi96ELb1EEv9LayerArgsS0_i
    .private_segment_fixed_size: 0
    .sgpr_count:     52
    .sgpr_spill_count: 0
    .symbol:         _Z10k_layer_fhILi96ELb1EEv9LayerArgsS0_i.kd
    .uniform_work_group_size: 1
    .uses_dynamic_stack: false
    .vgpr_count:     168
    .vgpr_spill_count: 0
    .wavefront_size: 64
  - .agpr_count:     0
    .args:
      - .offset:         0
        .size:           104
        .value_kind:     by_value
      - .offset:         104
        .size:           104
        .value_kind:     by_value
      - .offset:         208
        .size:           4
        .value_kind:     by_value
      - .offset:         216
        .size:           4
        .value_kind:     hidden_block_count_x
      - .offset:         220
        .size:           4
        .value_kind:     hidden_block_count_y
      - .offset:         224
        .size:           4
        .value_kind:     hidden_block_count_z
      - .offset:         228
        .size:           2
        .value_kind:     hidden_group_size_x
      - .offset:         230
        .size:           2
        .value_kind:     hidden_group_size_y
      - .offset:         232
        .size:           2
        .value_kind:     hidden_group_size_z
      - .offset:         234
        .size:           2
        .value_kind:     hidden_remainder_x
      - .offset:         236
        .size:           2
        .value_kind:     hidden_remainder_y
      - .offset:         238
        .size:           2
        .value_kind:     hidden_remainder_z
      - .offset:         256
        .size:           8
        .value_kind:     hidden_global_offset_x
      - .offset:         264
        .size:           8
        .value_kind:     hidden_global_offset_y
      - .offset:         272
        .size:           8
        .value_kind:     hidden_global_offset_z
      - .offset:         280
        .size:           2
        .value_kind:     hidden_grid_dims
    .group_segment_fixed_size: 151044
    .kernarg_segment_align: 8
    .kernarg_segment_size: 472
    .language:       OpenCL C
    .language_version:
      - 2
      - 0
    .max_flat_workgroup_size: 768
    .name:           _Z10k_layer_fhILi128ELb1EEv9LayerArgsS0_i
    .private_segment_fixed_size: 0
    .sgpr_count:     45
    .sgpr_spill_count: 0
    .symbol:         _Z10k_layer_fhILi128ELb1EEv9LayerArgsS0_i.kd
    .uniform_work_group_size: 1
    .uses_dynamic_stack: false
    .vgpr_count:     168
    .vgpr_spill_count: 0
    .wavefront_size: 64
